# speedup vs baseline: 1.0161x; 1.0161x over previous
_Z14moe_persistent8GemmArgs:
	s_load_dwordx8 s[24:31], s[0:1], 0x0
	s_load_dwordx2 s[4:5], s[0:1], 0x20
	s_load_dwordx16 s[8:23], s[0:1], 0x70
	v_mov_b32_e32 v1, 0
	v_mov_b32_e32 v245, 0
	v_cmp_eq_u32_e64 s[6:7], 0, v0
	s_waitcnt lgkmcnt(0)
	v_writelane_b32 v244, s4, 0
	s_nop 1
	v_writelane_b32 v244, s5, 1
	s_and_saveexec_b64 s[4:5], s[6:7]
	s_cbranch_execz .LBB2_4
	s_load_dwordx2 s[44:45], s[0:1], 0x28
	v_mov_b32_e32 v2, 0
	s_mov_b64 s[34:35], exec
	s_waitcnt lgkmcnt(0)
	s_load_dwordx8 s[36:43], s[44:45], 0x0
	s_waitcnt lgkmcnt(0)
	s_add_i32 s3, s36, 0xff
	s_add_i32 s33, s37, 0xff
	s_add_i32 s44, s38, 0xff
	s_add_i32 s45, s39, 0xff
	s_ashr_i32 s33, s33, 8
	s_ashr_i32 s3, s3, 8
	s_ashr_i32 s47, s45, 8
	s_mul_i32 s48, s3, 0x2a8
	s_add_i32 s49, s33, s3
	s_ashr_i32 s44, s44, 8
	v_mov_b32_e32 v6, s3
	s_add_i32 s3, 0, 0x20820
	s_add_i32 s51, s44, s49
	v_mov_b32_e32 v7, s33
	v_mov_b32_e32 v8, s44
	v_mov_b32_e32 v9, s47
	v_mov_b32_e32 v1, s3
	s_add_i32 s3, 0, 0x20840
	ds_write_b128 v1, v[6:9]
	v_mov_b32_e32 v4, s49
	v_mov_b32_e32 v5, s51
	v_mov_b32_e32 v3, v6
	v_mov_b32_e32 v1, s3
	ds_write_b128 v1, v[2:5]
	v_mov_b32_e32 v4, s36
	s_add_i32 s3, 0, 0x20860
	s_add_i32 s36, s40, 0xff
	s_mul_i32 s50, s33, 0x2a8
	v_mov_b32_e32 v5, s37
	v_mov_b32_e32 v6, s38
	v_mov_b32_e32 v7, s39
	v_mov_b32_e32 v1, s3
	s_add_i32 s3, s47, s51
	s_mul_i32 s33, s47, 0x2a8
	s_add_i32 s37, s41, 0xff
	s_ashr_i32 s36, s36, 8
	s_add_i32 s47, s42, 0xff
	s_add_i32 s51, s43, 0xff
	s_mul_i32 s52, s44, 0x2a8
	ds_write_b128 v1, v[4:7]
	s_ashr_i32 s37, s37, 8
	s_add_i32 s38, s36, s3
	s_mul_i32 s44, s36, 0x2a8
	s_ashr_i32 s51, s51, 8
	s_ashr_i32 s47, s47, 8
	v_mov_b32_e32 v4, s36
	s_add_i32 s36, 0, 0x20830
	s_add_i32 s39, s37, s38
	v_mov_b32_e32 v5, s37
	v_mov_b32_e32 v6, s47
	v_mov_b32_e32 v7, s51
	v_mov_b32_e32 v1, s36
	s_add_i32 s53, s47, s39
	ds_write_b128 v1, v[4:7]
	v_mov_b32_e32 v4, s3
	s_add_i32 s3, 0, 0x20850
	s_mul_i32 s49, s37, 0x2a8
	s_mul_i32 s54, s47, 0x2a8
	v_mov_b32_e32 v5, s38
	v_mov_b32_e32 v6, s39
	v_mov_b32_e32 v7, s53
	v_mov_b32_e32 v1, s3
	s_add_i32 s3, 0, 0x20870
	ds_write_b128 v1, v[4:7]
	v_mov_b32_e32 v1, s3
	s_add_i32 s3, s50, s52
	s_add_i32 s36, s33, s44
	s_add_i32 s37, s49, s54
	s_add_i32 s3, s48, s3
	s_add_i32 s36, s36, s37
	s_add_i32 s3, s3, s36
	s_and_b32 s99, s2, 7
	s_lshl_b32 s36, s2, 5
	s_and_b32 s36, s36, 0xe0
	s_lshr_b32 s2, s2, 3
	v_mov_b32_e32 v4, s40
	s_mul_i32 s40, s51, 0x2a8
	s_add_i32 s36, s36, s2
	s_add_i32 s46, s48, 0x4b0
	s_add_i32 s3, s3, s40
	s_lshl_b32 s2, s36, 1
	s_addk_i32 s3, 0x2580
	s_or_b32 s2, s2, 1
	s_ashr_i32 s47, s46, 31
	s_addk_i32 s50, 0x4b0
	s_mul_hi_i32 s37, s3, s2
	s_mul_i32 s36, s3, s2
	s_lshl_b64 s[2:3], s[46:47], 9
	s_ashr_i32 s39, s50, 31
	s_add_u32 s38, s50, s46
	v_mov_b32_e32 v5, s41
	v_mov_b32_e32 v6, s42
	v_mov_b32_e32 v7, s43
	s_addc_u32 s39, s39, s47
	ds_write_b128 v1, v[4:7]
	v_mov_b64_e32 v[4:5], s[2:3]
	s_lshl_b64 s[2:3], s[38:39], 9
	v_cmp_ge_i64_e32 vcc, s[36:37], v[4:5]
	v_mov_b64_e32 v[4:5], s[2:3]
	v_cmp_lt_i64_e64 s[2:3], s[36:37], v[4:5]
	s_and_b64 s[2:3], vcc, s[2:3]
	s_addk_i32 s52, 0x4b0
	v_cndmask_b32_e64 v1, 0, 1, s[2:3]
	s_ashr_i32 s2, s52, 31
	s_add_u32 s38, s38, s52
	s_addc_u32 s39, s39, s2
	s_lshl_b64 s[2:3], s[38:39], 9
	v_cmp_ge_i64_e32 vcc, s[36:37], v[4:5]
	v_mov_b64_e32 v[4:5], s[2:3]
	v_cmp_lt_i64_e64 s[2:3], s[36:37], v[4:5]
	s_and_b64 s[2:3], vcc, s[2:3]
	s_and_b64 s[2:3], s[2:3], exec
	v_readfirstlane_b32 s2, v1
	s_cselect_b32 s41, 2, s2
	s_addk_i32 s33, 0x4b0
	s_ashr_i32 s2, s33, 31
	s_add_u32 s38, s38, s33
	s_addc_u32 s39, s39, s2
	s_lshl_b64 s[2:3], s[38:39], 9
	v_cmp_ge_i64_e32 vcc, s[36:37], v[4:5]
	v_mov_b64_e32 v[4:5], s[2:3]
	v_cmp_lt_i64_e64 s[2:3], s[36:37], v[4:5]
	s_and_b64 s[2:3], vcc, s[2:3]
	s_and_b64 s[2:3], s[2:3], exec
	s_cselect_b32 s33, 3, s41
	s_addk_i32 s44, 0x4b0
	s_ashr_i32 s2, s44, 31
	s_add_u32 s38, s38, s44
	s_addc_u32 s39, s39, s2
	s_lshl_b64 s[2:3], s[38:39], 9
	v_cmp_ge_i64_e32 vcc, s[36:37], v[4:5]
	v_mov_b64_e32 v[4:5], s[2:3]
	v_cmp_lt_i64_e64 s[2:3], s[36:37], v[4:5]
	s_and_b64 s[2:3], vcc, s[2:3]
	s_and_b64 s[2:3], s[2:3], exec
	s_cselect_b32 s33, 4, s33
	s_addk_i32 s49, 0x4b0
	s_ashr_i32 s2, s49, 31
	s_add_u32 s38, s38, s49
	s_addc_u32 s39, s39, s2
	s_lshl_b64 s[2:3], s[38:39], 9
	v_cmp_ge_i64_e32 vcc, s[36:37], v[4:5]
	v_mov_b64_e32 v[4:5], s[2:3]
	v_cmp_lt_i64_e64 s[2:3], s[36:37], v[4:5]
	s_and_b64 s[2:3], vcc, s[2:3]
	s_and_b64 s[2:3], s[2:3], exec
	s_cselect_b32 s33, 5, s33
	s_addk_i32 s54, 0x4b0
	s_ashr_i32 s2, s54, 31
	s_add_u32 s38, s38, s54
	s_addc_u32 s39, s39, s2
	s_lshl_b64 s[2:3], s[38:39], 9
	v_cmp_ge_i64_e32 vcc, s[36:37], v[4:5]
	v_mov_b64_e32 v[4:5], s[2:3]
	v_cmp_lt_i64_e64 s[2:3], s[36:37], v[4:5]
	s_and_b64 s[2:3], vcc, s[2:3]
	s_and_b64 s[2:3], s[2:3], exec
	s_cselect_b32 s33, 6, s33
	s_addk_i32 s40, 0x4b0
	s_ashr_i32 s3, s40, 31
	s_add_u32 s2, s38, s40
	s_addc_u32 s3, s39, s3
	s_lshl_b64 s[2:3], s[2:3], 9
	v_cmp_ge_i64_e32 vcc, s[36:37], v[4:5]
	v_mov_b64_e32 v[4:5], s[2:3]
	v_cmp_lt_i64_e64 s[2:3], s[36:37], v[4:5]
	s_and_b64 s[2:3], vcc, s[2:3]
	s_and_b64 s[2:3], s[2:3], exec
	s_cselect_b32 s44, 7, s33
	s_mov_b32 s44, s99
	s_add_i32 s2, 0, 0x20880
	v_mov_b32_e32 v3, v2
	v_mov_b32_e32 v1, s2
	s_add_i32 s2, 0, 0x20808
	ds_write_b64 v1, v[2:3]
	v_mov_b32_e32 v1, s2
	v_mov_b32_e32 v3, s44
	ds_write_b32 v1, v3
	v_mbcnt_lo_u32_b32 v1, s34, 0
	v_mbcnt_hi_u32_b32 v1, s35, v1
	s_mov_b32 s45, 0
	v_cmp_eq_u32_e32 vcc, 0, v1
	s_and_saveexec_b64 s[2:3], vcc
	s_cbranch_execz .LBB2_3
	s_lshl_b64 s[36:37], s[44:45], 2
	s_add_u32 s36, s10, s36
	s_addc_u32 s37, s11, s37
	s_bcnt1_i32_b64 s33, s[34:35]
	v_mov_b32_e32 v3, s33
	global_atomic_add v3, v2, v3, s[36:37] sc0

.LBB2_6:
.LBB2_7:
	s_barrier
	s_and_saveexec_b64 s[2:3], s[6:7]
	s_cbranch_execz .LBB2_270
	v_add_u32_e32 v1, v245, v1
	s_sub_u32 s53, s77, s76
	s_lshr_b32 s53, s53, 2
	s_lshl_b32 s0, s53, 2
	s_sub_u32 s56, s78, s0
	s_subb_u32 s57, s79, 0
	s_mov_b32 s54, 0
	v_readfirstlane_b32 s52, v1
.Lsched_scan:
	s_add_u32 s55, s53, s54
	s_and_b32 s55, s55, 7
	s_lshl_b32 s0, s55, 2
	s_add_u32 s1, s76, s0
	v_mov_b32_e32 v2, s1
	ds_read_b32 v2, v2 offset:32
	s_waitcnt lgkmcnt(0)
	v_readfirstlane_b32 s33, v2
	s_mul_i32 s34, s33, 17
	s_addk_i32 s34, 0x50
	s_cmp_eq_u32 s54, 0
	s_cbranch_scc1 .Lsched_have_h
	v_mov_b32_e32 v2, s0
	global_load_dword v3, v2, s[56:57] sc1
	s_waitcnt vmcnt(0)
	v_readfirstlane_b32 s1, v3
	s_cmp_ge_i32 s1, s34
	s_cbranch_scc1 .Lsched_next
	v_mov_b32_e32 v3, 1
	global_atomic_add v3, v2, v3, s[56:57] sc0
	s_waitcnt vmcnt(0)
	v_readfirstlane_b32 s52, v3
.Lsched_have_h:
	s_cmp_lt_i32 s52, s34
	s_cbranch_scc1 .Lsched_decode
.Lsched_next:
	s_add_u32 s54, s54, 1
	s_cmp_lt_u32 s54, 8
	s_cbranch_scc1 .Lsched_scan
	s_mov_b32 s35, -1
	s_mov_b32 s55, 0
	s_branch .Lsched_store
.Lsched_decode:
	s_cmp_lt_u32 s52, 12
	s_cbranch_scc0 .Lsched_d1
	s_lshr_b32 s0, s52, 2
	s_lshl_b32 s0, s0, 4
	s_and_b32 s1, s52, 3
	s_or_b32 s35, s0, s1
	s_or_b32 s35, s35, 0x2000000
	s_branch .Lsched_store
.Lsched_d1:
	s_sub_u32 s52, s52, 12
	s_min_u32 s86, s33, 0
	s_mul_i32 s87, s86, 3
	s_cmp_lt_u32 s52, s87
	s_cbranch_scc0 .Lsched_d2
	s_mul_i32 s0, s52, 171
	s_lshr_b32 s0, s0, 9
	s_mul_i32 s1, s0, 3
	s_sub_u32 s1, s52, s1
	s_lshl_b32 s0, s0, 8
	s_lshl_b32 s1, s1, 4
	s_or_b32 s35, s0, s1
	s_branch .Lsched_store
.Lsched_d2:
	s_sub_u32 s52, s52, s87
	s_cmp_lt_u32 s52, 20
	s_cbranch_scc0 .Lsched_d3
	s_lshr_b32 s0, s52, 2
	s_add_u32 s0, s0, 3
	s_lshl_b32 s0, s0, 4
	s_and_b32 s1, s52, 3
	s_or_b32 s35, s0, s1
	s_or_b32 s35, s35, 0x2000000
	s_branch .Lsched_store
.Lsched_d3:
	s_sub_u32 s52, s52, 20
	s_lshl_b32 s88, s33, 3
	s_sub_u32 s89, s88, s87
	s_add_u32 s90, s33, 16
	s_add_u32 s91, s89, s90
	s_cmp_lt_u32 s52, s91
	s_cbranch_scc0 .Lsched_d6
	s_lshr_b32 s0, s89, 1
	s_min_u32 s0, s0, s90
	s_mul_i32 s1, s0, 3
	s_cmp_lt_u32 s52, s1
	s_cbranch_scc0 .Lsched_d4
	s_mul_i32 s93, s52, 43691
	s_lshr_b32 s93, s93, 17
	s_mul_i32 s1, s93, 3
	s_sub_u32 s1, s52, s1
	s_cmp_lt_u32 s1, 2
	s_cbranch_scc0 .Lsched_pb
	s_lshl_b32 s92, s93, 1
	s_add_u32 s92, s92, s1
	s_branch .Lsched_isa
.Lsched_pb:
	s_mov_b32 s92, s93
	s_branch .Lsched_isb
.Lsched_d4:
	s_sub_u32 s1, s52, s1
	s_lshl_b32 s93, s0, 1
	s_sub_u32 s93, s89, s93
	s_cmp_lt_u32 s1, s93
	s_cbranch_scc0 .Lsched_d5
	s_lshl_b32 s92, s0, 1
	s_add_u32 s92, s92, s1
	s_branch .Lsched_isa
.Lsched_d5:
	s_sub_u32 s1, s1, s93
	s_add_u32 s92, s0, s1
.Lsched_isb:
	s_cmp_lt_u32 s92, 16
	s_cbranch_scc0 .Lsched_lora
	s_lshr_b32 s0, s92, 1
	s_lshl_b32 s0, s0, 4
	s_and_b32 s1, s92, 1
	s_or_b32 s35, s0, s1
	s_or_b32 s35, s35, 0x3000000
	s_branch .Lsched_store
.Lsched_lora:
	s_sub_u32 s0, s92, 16
	s_lshl_b32 s0, s0, 8
	s_or_b32 s35, s0, 0x4000000
	s_branch .Lsched_store
.Lsched_isa:
	s_mul_i32 s0, s86, 5
	s_cmp_lt_u32 s92, s0
	s_cbranch_scc0 .Lsched_a2
	s_mul_i32 s1, s92, 205
	s_lshr_b32 s1, s1, 10
	s_mul_i32 s0, s1, 5
	s_sub_u32 s0, s92, s0
	s_add_u32 s0, s0, 3
	s_lshl_b32 s1, s1, 8
	s_lshl_b32 s0, s0, 4
	s_or_b32 s35, s1, s0
	s_branch .Lsched_store
.Lsched_a2:
	s_sub_u32 s92, s92, s0
	s_lshr_b32 s1, s92, 3
	s_add_u32 s1, s1, s86
	s_and_b32 s0, s92, 7
	s_lshl_b32 s1, s1, 8
	s_lshl_b32 s0, s0, 4
	s_or_b32 s35, s1, s0
	s_branch .Lsched_store
.Lsched_d6:
	s_sub_u32 s52, s52, s91
	s_cmp_lt_u32 s52, s88
	s_cbranch_scc0 .Lsched_d7
	s_lshr_b32 s1, s52, 3
	s_and_b32 s0, s52, 7
	s_lshl_b32 s1, s1, 8
	s_lshl_b32 s0, s0, 4
	s_or_b32 s35, s1, s0
	s_or_b32 s35, s35, 0x1000000
	s_branch .Lsched_store
.Lsched_d7:
	s_sub_u32 s52, s52, s88
	s_lshl_b32 s0, s52, 3
	s_add_u32 s0, s0, s55
	s_lshl_b32 s0, s0, 8
	s_or_b32 s35, s0, 0x5000000
.Lsched_store:
	v_mov_b32_e32 v2, s35
	v_mov_b32_e32 v3, s55
	v_mov_b32_e32 v4, s76
	ds_write_b64 v4, v[2:3]

.LBB2_311:
	s_andn2_b64 vcc, exec, s[2:3]
	s_cbranch_vccnz .LBB2_368
	v_mov_b32_e32 v148, v0
	s_nop 0
	v_ashrrev_i32_e32 v149, 6, v148
	v_cmp_eq_u32_e64 s[2:3], 0, v148
	v_readfirstlane_b32 s33, v149
	s_lshl_b32 s100, s55, 8
	s_sub_u32 s100, s86, s100
	s_sub_u32 s100, s100, 1
	s_cmp_ge_u32 s100, 255
	s_cbranch_scc1 .Lg2_full
	s_lshr_b32 s101, s33, 2
	s_lshl_b32 s101, s101, 6
	s_sub_i32 s101, s100, s101
	s_lshr_b32 s100, s101, 31
	s_cmp_lt_i32 s101, 0x80
	s_cselect_b32 s101, 2, 0
	s_or_b32 s100, s100, s101
	s_or_b32 s100, s100, 4
	s_branch .Lg2_flags_done
.Lg2_full:
	s_mov_b32 s100, 0
.Lg2_flags_done:
	s_and_saveexec_b64 s[4:5], s[2:3]
	s_cbranch_execz .LBB2_329
	v_readlane_b32 s10, v244, 51
	s_lshl_b32 s52, 1, s0
	s_nop 0
	v_mov_b32_e32 v2, s10
	ds_read_b32 v2, v2
	s_waitcnt lgkmcnt(0)
	v_and_b32_e32 v2, s52, v2
	v_cmp_ne_u32_e32 vcc, 0, v2
	s_cbranch_vccnz .LBB2_329
	s_ashr_i32 s97, s96, 31
	s_lshl_b64 s[10:11], s[96:97], 2
	s_add_u32 s88, s8, s10
	v_mov_b32_e32 v2, s34
	s_addc_u32 s89, s9, s11
	s_lshl_b32 s34, s0, 3
	s_ashr_i32 s35, s34, 31
	s_lshl_b64 s[34:35], s[34:35], 2
	s_add_u32 s56, s14, s34
	s_addc_u32 s57, s15, s35
	s_lshl_b32 s53, s54, 2
	s_add_u32 s34, s56, s53
	s_addc_u32 s35, s57, 0
	v_mov_b32_e32 v3, s53
	s_add_u32 s10, s16, s10
	ds_read_b32 v2, v2 offset:32
	global_load_dword v6, v163, s[88:89] sc1
	global_load_dword v5, v3, s[56:57] sc1
	s_addc_u32 s11, s17, s11
	s_lshl_b64 s[56:57], s[0:1], 2
	s_add_u32 s56, s20, s56
	s_addc_u32 s57, s21, s57
	global_load_dword v4, v163, s[10:11] sc1
	global_load_dword v3, v163, s[56:57] sc1
	s_waitcnt vmcnt(3)
	v_cmp_lt_i32_e32 vcc, 7, v6
	s_cbranch_vccnz .LBB2_318
	global_load_dword v6, v163, s[88:89] sc1
	s_waitcnt vmcnt(0)
	v_cmp_lt_i32_e32 vcc, 7, v6
	s_cbranch_vccnz .LBB2_318
	s_mov_b32 s53, 0

.LBB2_355:
	s_or_b64 exec, exec, s[52:53]
	s_add_u32 s52, s92, 0x80
	s_addc_u32 s53, s93, 0
	s_add_i32 s82, 0, 0x18000
	s_add_i32 s58, s82, s57
	s_waitcnt vmcnt(0)
	v_mfma_f32_16x16x32_f16 v[102:105], v[6:9], v[30:33], 0
	s_mov_b32 m0, s58
	s_waitcnt vmcnt(4)
	s_barrier
	v_mfma_f32_16x16x32_f16 v[98:101], v[6:9], v[26:29], 0
	v_mfma_f32_16x16x32_f16 v[126:129], v[2:5], v[30:33], 0
	v_mfma_f32_16x16x32_f16 v[122:125], v[2:5], v[26:29], 0
	v_mfma_f32_16x16x32_f16 v[118:121], v[14:17], v[30:33], 0
	v_mfma_f32_16x16x32_f16 v[110:113], v[10:13], v[30:33], 0
	v_mfma_f32_16x16x32_f16 v[94:97], v[6:9], v[142:145], 0
	v_mfma_f32_16x16x32_f16 v[90:93], v[6:9], v[138:141], 0
	v_mfma_f32_16x16x32_f16 v[86:89], v[2:5], v[142:145], 0
	v_mfma_f32_16x16x32_f16 v[82:85], v[2:5], v[138:141], 0
	v_mfma_f32_16x16x32_f16 v[62:65], v[22:25], v[30:33], 0
	v_mfma_f32_16x16x32_f16 v[54:57], v[18:21], v[30:33], 0
	v_mfma_f32_16x16x32_f16 v[46:49], v[134:137], v[30:33], 0
	v_mfma_f32_16x16x32_f16 v[38:41], v[130:133], v[30:33], 0
	v_mfma_f32_16x16x32_f16 v[30:33], v[130:133], v[26:29], 0
	v_mfma_f32_16x16x32_f16 v[6:9], v[130:133], v[142:145], 0
	v_mfma_f32_16x16x32_f16 v[2:5], v[130:133], v[138:141], 0
	v_lshl_add_u64 v[130:131], s[52:53], 0, v[162:163]
	s_add_u32 s52, s52, 0x20000
	global_load_lds_dwordx4 v[130:131], off
	s_addc_u32 s53, s53, 0
	s_add_i32 m0, s58, 0x2000
	s_add_u32 s58, s90, 0x80
	s_addc_u32 s59, s91, 0
	v_lshl_add_u64 v[130:131], s[52:53], 0, v[162:163]
	s_add_i32 s52, s97, 0x8000
	global_load_lds_dwordx4 v[130:131], off
	v_lshl_add_u64 v[130:131], s[58:59], 0, v[162:163]
	s_add_u32 s58, s58, 0x20000
	s_addc_u32 s59, s59, 0
	s_mov_b32 m0, s52
	s_add_i32 s53, s97, 0xa000
	global_load_lds_dwordx4 v[130:131], off
	v_lshl_add_u64 v[130:131], s[58:59], 0, v[162:163]
	s_add_u32 s58, s92, 0x40080
	s_addc_u32 s59, s93, 0
	s_add_i32 s83, 0, 0x1c000
	s_mov_b32 m0, s53
	s_add_i32 s57, s83, s57
	global_load_lds_dwordx4 v[130:131], off
	v_lshl_add_u64 v[130:131], s[58:59], 0, v[162:163]
	s_add_u32 s58, s58, 0x20000
	s_mov_b32 m0, s57
	s_addc_u32 s59, s59, 0
	global_load_lds_dwordx4 v[130:131], off
	s_add_i32 m0, s57, 0x2000
	v_lshl_add_u64 v[130:131], s[58:59], 0, v[162:163]
	global_load_lds_dwordx4 v[130:131], off
	v_lshlrev_b32_e32 v132, 2, v152
	v_lshlrev_b32_e32 v130, 6, v152
	v_and_b32_e32 v131, 32, v132
	v_bitop3_b32 v130, v130, v131, v146 bitop3:0x36
	s_add_i32 s57, 0, 0x10000
	v_add_u32_e32 v131, s57, v130
	s_add_i32 s57, 0, 0x14000
	v_mfma_f32_16x16x32_f16 v[114:117], v[14:17], v[26:29], 0
	s_waitcnt vmcnt(6)
	v_lshlrev_b32_e32 v133, 13, v154
	s_barrier
	v_mfma_f32_16x16x32_f16 v[106:109], v[10:13], v[26:29], 0
	v_mfma_f32_16x16x32_f16 v[78:81], v[14:17], v[142:145], 0
	v_mfma_f32_16x16x32_f16 v[74:77], v[14:17], v[138:141], 0
	v_mfma_f32_16x16x32_f16 v[70:73], v[10:13], v[142:145], 0
	v_mfma_f32_16x16x32_f16 v[66:69], v[10:13], v[138:141], 0
	v_mfma_f32_16x16x32_f16 v[58:61], v[22:25], v[26:29], 0
	v_mfma_f32_16x16x32_f16 v[50:53], v[18:21], v[26:29], 0
	v_mfma_f32_16x16x32_f16 v[42:45], v[134:137], v[26:29], 0
	v_mfma_f32_16x16x32_f16 v[34:37], v[22:25], v[142:145], 0
	v_mfma_f32_16x16x32_f16 v[26:29], v[22:25], v[138:141], 0
	v_mfma_f32_16x16x32_f16 v[22:25], v[18:21], v[142:145], 0
	v_mfma_f32_16x16x32_f16 v[18:21], v[18:21], v[138:141], 0
	v_mfma_f32_16x16x32_f16 v[14:17], v[134:137], v[142:145], 0
	v_mfma_f32_16x16x32_f16 v[10:13], v[134:137], v[138:141], 0
	v_add_u32_e32 v136, s57, v130
	v_add_u32_e32 v139, s82, v130
	v_add_u32_e32 v140, s83, v130
	v_or_b32_e32 v130, v151, v152
	v_lshlrev_b32_e32 v134, 6, v130
	s_movk_i32 s57, 0x3c0
	v_lshlrev_b32_e32 v130, 2, v130
	v_and_or_b32 v134, v134, s57, v146
	v_and_b32_e32 v130, 32, v130
	v_xad_u32 v130, v134, v130, 0
	v_or_b32_e32 v134, 16, v151
	v_or_b32_e32 v137, v134, v152
	v_lshlrev_b32_e32 v138, 6, v137
	v_lshlrev_b32_e32 v137, 2, v137
	v_and_or_b32 v138, v138, s57, v146
	v_and_b32_e32 v137, 32, v137
	v_lshlrev_b32_e32 v141, 7, v134
	v_or_b32_e32 v134, 32, v151
	v_xad_u32 v137, v138, v137, 0
	v_or_b32_e32 v138, v134, v152
	v_lshlrev_b32_e32 v142, 6, v138
	v_lshlrev_b32_e32 v138, 2, v138
	v_and_or_b32 v142, v142, s57, v146
	v_and_b32_e32 v138, 32, v138
	v_lshlrev_b32_e32 v143, 7, v134
	v_or_b32_e32 v134, 48, v151
	v_xad_u32 v142, v142, v138, 0
	v_or_b32_e32 v138, v134, v152
	v_lshlrev_b32_e32 v144, 6, v138
	v_lshlrev_b32_e32 v138, 2, v138
	v_and_or_b32 v144, v144, s57, v146
	v_and_b32_e32 v138, 32, v138
	v_lshlrev_b32_e32 v135, 12, v153
	v_xad_u32 v144, v144, v138, 0
	v_lshlrev_b32_e32 v145, 7, v134
	s_mov_b32 s57, 0
	v_add_u32_e32 v138, v131, v135
	v_add_u32_e32 v134, v130, v133
	v_add_u32_e32 v133, v137, v141
	v_add_u32_e32 v131, v142, v143
	v_add_u32_e32 v130, v144, v145
	v_add_u32_e32 v137, v136, v135
	v_add_u32_e32 v136, v139, v135
	v_add_u32_e32 v135, v140, v135
	s_cmp_lg_u32 s100, 0
	s_cbranch_scc1 .Lg2p_loop

.Lg2_join:
	s_movk_i32 s11, 0x100
	v_cmp_gt_u32_e32 vcc, s11, v148
	s_barrier
	s_and_saveexec_b64 s[34:35], vcc
	s_cbranch_execz .LBB2_359
	s_barrier

.LBB2_369:
	s_and_b64 vcc, exec, s[2:3]
	s_cbranch_vccz .LBB2_6
	v_mov_b32_e32 v141, v0
	s_add_i32 s86, s86, -1
	v_bfe_i32 v4, v141, 27, 1
	v_lshlrev_b32_e32 v2, 4, v141
	v_lshrrev_b32_e32 v4, 22, v4
	v_add_u32_e32 v4, v2, v4
	v_and_b32_e32 v4, 0xfffffc00, v4
	v_sub_u32_e32 v2, v2, v4
	v_ashrrev_i32_e32 v3, 31, v141
	v_lshrrev_b32_e32 v4, 4, v2
	v_lshrrev_b32_e32 v3, 26, v3
	v_bitop3_b32 v4, v4, v2, 32 bitop3:0x6c
	v_add_u32_e32 v3, v141, v3
	v_ashrrev_i32_e32 v5, 31, v4
	v_ashrrev_i32_e32 v3, 6, v3
	v_lshrrev_b32_e32 v5, 26, v5
	v_lshlrev_b32_e32 v2, 3, v3
	v_add_u32_e32 v5, v4, v5
	v_and_b32_e32 v2, -16, v2
	v_ashrrev_i32_e32 v5, 6, v5
	v_add_u32_e32 v2, v5, v2
	v_lshl_add_u32 v12, s55, 8, v2
	v_add_u32_e32 v8, 64, v12
	s_lshl_b32 s2, s0, 13
	v_min_i32_e32 v6, s86, v12
	v_min_i32_e32 v8, s86, v8
	v_add_u32_e32 v10, 0x80, v12
	v_add_u32_e32 v12, 0xc0, v12
	v_add_u32_e32 v6, s2, v6
	v_add_u32_e32 v8, s2, v8
	v_min_i32_e32 v10, s86, v10
	v_min_i32_e32 v12, s86, v12
	v_ashrrev_i32_e32 v7, 31, v6
	v_ashrrev_i32_e32 v9, 31, v8
	v_add_u32_e32 v10, s2, v10
	v_add_u32_e32 v12, s2, v12
	v_lshl_add_u64 v[6:7], v[6:7], 2, s[36:37]
	v_lshl_add_u64 v[8:9], v[8:9], 2, s[36:37]
	v_ashrrev_i32_e32 v11, 31, v10
	v_ashrrev_i32_e32 v13, 31, v12
	v_lshl_add_u64 v[10:11], v[10:11], 2, s[36:37]
	v_lshl_add_u64 v[12:13], v[12:13], 2, s[36:37]
	global_load_dword v6, v[6:7], off
	s_nop 0
	global_load_dword v7, v[8:9], off
	s_nop 0
	global_load_dword v8, v[10:11], off
	global_load_dword v9, v[12:13], off
	v_ashrrev_i32_e32 v138, 6, v141
	v_cmp_eq_u32_e64 s[2:3], 0, v141
	v_readfirstlane_b32 s33, v138
	s_lshl_b32 s100, s55, 8
	s_sub_u32 s100, s86, s100
	s_cmp_ge_u32 s100, 255
	s_cbranch_scc1 .Lg1_full
	s_lshr_b32 s101, s33, 2
	s_lshl_b32 s101, s101, 6
	s_sub_i32 s101, s100, s101
	s_lshr_b32 s100, s101, 31
	s_cmp_lt_i32 s101, 0x80
	s_cselect_b32 s101, 2, 0
	s_or_b32 s100, s100, s101
	s_or_b32 s100, s100, 4
	s_branch .Lg1_flags_done

.Lg1_flags_done:
	s_and_saveexec_b64 s[4:5], s[2:3]
	s_cbranch_execz .LBB2_379
	v_readlane_b32 s10, v244, 52
	s_lshl_b32 s34, 1, s0
	s_nop 0
	v_mov_b32_e32 v10, s10
	ds_read_b32 v10, v10
	s_waitcnt lgkmcnt(0)
	v_and_b32_e32 v10, s34, v10
	v_cmp_ne_u32_e32 vcc, 0, v10
	s_cbranch_vccnz .LBB2_379
	s_lshl_b32 s10, s0, 3
	s_ashr_i32 s11, s10, 31
	s_lshl_b64 s[10:11], s[10:11], 2
	s_add_u32 s52, s12, s10
	s_addc_u32 s53, s13, s11
	s_lshl_b32 s35, s54, 2
	s_add_u32 s10, s52, s35
	v_mov_b32_e32 v10, s35
	s_addc_u32 s11, s53, 0
	global_load_dword v11, v10, s[52:53] sc1
	s_lshl_b64 s[52:53], s[0:1], 2
	s_add_u32 s52, s18, s52
	s_addc_u32 s53, s19, s53
	global_load_dword v10, v163, s[52:53] sc1
	s_waitcnt vmcnt(1)
	v_cmp_lt_i32_e32 vcc, 3, v11
	s_cbranch_vccnz .LBB2_376
	global_load_dword v11, v163, s[10:11] sc1
	s_waitcnt vmcnt(0)
	v_cmp_lt_i32_e32 vcc, 3, v11
	s_cbranch_vccnz .LBB2_376
	s_mov_b32 s35, 0

.LBB2_381:
	s_or_b64 exec, exec, s[34:35]
	s_add_u32 s34, s4, 0x80
	s_addc_u32 s35, s5, 0
	s_add_i32 s58, 0, 0x18000
	s_add_i32 s56, s58, s33
	v_lshl_add_u64 v[4:5], s[34:35], 0, v[162:163]
	s_add_u32 s34, s34, 0x40000
	s_mov_b32 m0, s56
	s_addc_u32 s35, s35, 0
	s_waitcnt vmcnt(4)
	s_barrier
	global_load_lds_dwordx4 v[4:5], off
	s_add_i32 m0, s56, 0x2000
	v_readlane_b32 s56, v244, 6
	v_mov_b32_e32 v135, v163
	v_lshl_add_u64 v[4:5], s[34:35], 0, v[162:163]
	v_readlane_b32 s57, v244, 7
	s_add_i32 s34, s52, 0x8000
	v_mov_b32_e32 v137, v163
	global_load_lds_dwordx4 v[4:5], off
	s_mov_b32 m0, s34
	v_lshl_add_u64 v[4:5], s[56:57], 0, v[134:135]
	s_add_i32 s35, s52, 0xa000
	global_load_lds_dwordx4 v[4:5], off
	v_lshl_add_u64 v[4:5], s[56:57], 0, v[136:137]
	s_add_u32 s56, s4, 0x80080
	s_addc_u32 s57, s5, 0
	s_add_i32 s59, 0, 0x1c000
	s_mov_b32 m0, s35
	s_add_i32 s33, s59, s33
	global_load_lds_dwordx4 v[4:5], off
	v_lshl_add_u64 v[4:5], s[56:57], 0, v[162:163]
	s_add_u32 s56, s56, 0x40000
	s_mov_b32 m0, s33
	s_addc_u32 s57, s57, 0
	global_load_lds_dwordx4 v[4:5], off
	s_add_i32 m0, s33, 0x2000
	v_lshl_add_u64 v[4:5], s[56:57], 0, v[162:163]
	global_load_lds_dwordx4 v[4:5], off
	v_and_b32_e32 v139, 15, v141
	v_bfe_u32 v140, v141, 4, 2
	v_lshlrev_b32_e32 v6, 2, v141
	v_lshlrev_b32_e32 v4, 4, v140
	v_lshlrev_b32_e32 v5, 6, v139
	v_and_b32_e32 v6, 32, v6
	v_bitop3_b32 v5, v4, v6, v5 bitop3:0x36
	s_add_i32 s33, 0, 0x10000
	v_add_u32_e32 v7, s33, v5
	s_add_i32 s33, 0, 0x14000
	v_lshlrev_b32_e32 v143, 6, v2
	v_add_u32_e32 v8, s33, v5
	v_lshlrev_b32_e32 v11, 13, v2
	v_lshlrev_b32_e32 v2, 6, v141
	s_movk_i32 s33, 0x3c0
	v_and_b32_e32 v142, 3, v138
	s_waitcnt vmcnt(6)
	v_and_or_b32 v2, v2, s33, v4
	v_lshlrev_b32_e32 v3, 12, v142
	v_add_u32_e32 v9, s58, v5
	v_add_u32_e32 v10, s59, v5
	v_add_u32_e32 v5, 0, v5
	v_xad_u32 v4, v2, v6, 0
	v_or_b32_e32 v6, 0x800, v11
	v_or_b32_e32 v12, 0x1000, v11
	v_or_b32_e32 v13, 0x1800, v11
	v_mov_b32_e32 v2, 0
	s_mov_b32 s84, 0
	v_add_u32_e32 v151, v7, v3
	v_add_u32_e32 v147, v5, v11
	v_add_u32_e32 v146, v4, v6
	v_add_u32_e32 v145, v4, v12
	v_add_u32_e32 v144, v4, v13
	v_add_u32_e32 v150, v8, v3
	v_add_u32_e32 v149, v9, v3
	v_add_u32_e32 v148, v10, v3
	v_mov_b32_e32 v3, v2
	v_mov_b32_e32 v4, v2
	v_mov_b32_e32 v5, v2
	v_mov_b32_e32 v6, v2
	v_mov_b32_e32 v7, v2
	v_mov_b32_e32 v8, v2
	v_mov_b32_e32 v9, v2
	v_mov_b32_e32 v10, v2
	v_mov_b32_e32 v11, v2
	v_mov_b32_e32 v12, v2
	v_mov_b32_e32 v13, v2
	v_mov_b32_e32 v14, v2
	v_mov_b32_e32 v15, v2
	v_mov_b32_e32 v16, v2
	v_mov_b32_e32 v17, v2
	v_mov_b32_e32 v18, v2
	v_mov_b32_e32 v19, v2
	v_mov_b32_e32 v20, v2
	v_mov_b32_e32 v21, v2
	v_mov_b32_e32 v22, v2
	v_mov_b32_e32 v23, v2
	v_mov_b32_e32 v24, v2
	v_mov_b32_e32 v25, v2
	v_mov_b32_e32 v26, v2
	v_mov_b32_e32 v27, v2
	v_mov_b32_e32 v28, v2
	v_mov_b32_e32 v29, v2
	v_mov_b32_e32 v30, v2
	v_mov_b32_e32 v31, v2
	v_mov_b32_e32 v32, v2
	v_mov_b32_e32 v33, v2
	v_mov_b32_e32 v34, v2
	v_mov_b32_e32 v35, v2
	v_mov_b32_e32 v36, v2
	v_mov_b32_e32 v37, v2
	v_mov_b32_e32 v38, v2
	v_mov_b32_e32 v39, v2
	v_mov_b32_e32 v40, v2
	v_mov_b32_e32 v41, v2
	v_mov_b32_e32 v42, v2
	v_mov_b32_e32 v43, v2
	v_mov_b32_e32 v44, v2
	v_mov_b32_e32 v45, v2
	v_mov_b32_e32 v46, v2
	v_mov_b32_e32 v47, v2
	v_mov_b32_e32 v48, v2
	v_mov_b32_e32 v49, v2
	v_mov_b32_e32 v50, v2
	v_mov_b32_e32 v51, v2
	v_mov_b32_e32 v52, v2
	v_mov_b32_e32 v53, v2
	v_mov_b32_e32 v54, v2
	v_mov_b32_e32 v55, v2
	v_mov_b32_e32 v56, v2
	v_mov_b32_e32 v57, v2
	v_mov_b32_e32 v58, v2
	v_mov_b32_e32 v59, v2
	v_mov_b32_e32 v60, v2
	v_mov_b32_e32 v61, v2
	v_mov_b32_e32 v62, v2
	v_mov_b32_e32 v63, v2
	v_mov_b32_e32 v64, v2
	v_mov_b32_e32 v65, v2
	v_mov_b32_e32 v66, v2
	v_mov_b32_e32 v67, v2
	v_mov_b32_e32 v68, v2
	v_mov_b32_e32 v69, v2
	v_mov_b32_e32 v70, v2
	v_mov_b32_e32 v71, v2
	v_mov_b32_e32 v72, v2
	v_mov_b32_e32 v73, v2
	v_mov_b32_e32 v74, v2
	v_mov_b32_e32 v75, v2
	v_mov_b32_e32 v76, v2
	v_mov_b32_e32 v77, v2
	v_mov_b32_e32 v78, v2
	v_mov_b32_e32 v79, v2
	v_mov_b32_e32 v80, v2
	v_mov_b32_e32 v81, v2
	v_mov_b32_e32 v82, v2
	v_mov_b32_e32 v83, v2
	v_mov_b32_e32 v84, v2
	v_mov_b32_e32 v85, v2
	v_mov_b32_e32 v86, v2
	v_mov_b32_e32 v87, v2
	v_mov_b32_e32 v88, v2
	v_mov_b32_e32 v89, v2
	v_mov_b32_e32 v90, v2
	v_mov_b32_e32 v91, v2
	v_mov_b32_e32 v92, v2
	v_mov_b32_e32 v93, v2
	v_mov_b32_e32 v94, v2
	v_mov_b32_e32 v95, v2
	v_mov_b32_e32 v96, v2
	v_mov_b32_e32 v97, v2
	v_mov_b32_e32 v98, v2
	v_mov_b32_e32 v99, v2
	v_mov_b32_e32 v100, v2
	v_mov_b32_e32 v101, v2
	v_mov_b32_e32 v102, v2
	v_mov_b32_e32 v103, v2
	v_mov_b32_e32 v104, v2
	v_mov_b32_e32 v105, v2
	v_mov_b32_e32 v106, v2
	v_mov_b32_e32 v107, v2
	v_mov_b32_e32 v108, v2
	v_mov_b32_e32 v109, v2
	v_mov_b32_e32 v110, v2
	v_mov_b32_e32 v111, v2
	v_mov_b32_e32 v112, v2
	v_mov_b32_e32 v113, v2
	v_mov_b32_e32 v114, v2
	v_mov_b32_e32 v115, v2
	v_mov_b32_e32 v116, v2
	v_mov_b32_e32 v117, v2
	v_mov_b32_e32 v118, v2
	v_mov_b32_e32 v119, v2
	v_mov_b32_e32 v120, v2
	v_mov_b32_e32 v121, v2
	v_mov_b32_e32 v122, v2
	v_mov_b32_e32 v123, v2
	v_mov_b32_e32 v124, v2
	v_mov_b32_e32 v125, v2
	v_mov_b32_e32 v126, v2
	v_mov_b32_e32 v127, v2
	v_mov_b32_e32 v128, v2
	v_mov_b32_e32 v129, v2
	v_mov_b32_e32 v133, v163
	v_mov_b32_e32 v131, v163
	s_barrier
	s_cmp_lg_u32 s100, 0
	s_cbranch_scc1 .Lg1p_loop

.Lg1_join:
	s_movk_i32 s4, 0x100
	v_cmp_gt_u32_e32 vcc, s4, v141
	s_barrier
	s_and_saveexec_b64 s[4:5], vcc
	s_cbranch_execz .LBB2_385
	s_barrier

.Lg1p_loop:
	ds_read_b128 v[152:155], v151
	ds_read_b128 v[156:159], v151 offset:1024
	ds_read_b128 v[164:167], v151 offset:2048
	ds_read_b128 v[168:171], v151 offset:3072
	s_lshl_b32 s58, s84, 7
	s_add_u32 s59, s24, s58
	s_addc_u32 s91, s25, 0
	s_add_u32 s92, s59, 0x80
	s_addc_u32 s93, s91, 0
	s_add_i32 s56, s52, 0xc000
	s_mov_b32 m0, s56
	v_lshl_add_u64 v[160:161], s[92:93], 0, v[132:133]
	s_add_i32 s33, s52, 0xe000
	ds_read_b128 v[172:175], v147
	ds_read_b128 v[176:179], v147 offset:1024
	ds_read_b128 v[184:187], v146
	ds_read_b128 v[188:191], v146 offset:1024
	ds_read_b128 v[192:195], v145
	ds_read_b128 v[196:199], v145 offset:1024
	ds_read_b128 v[200:203], v144
	ds_read_b128 v[204:207], v144 offset:1024
	global_load_lds_dwordx4 v[160:161], off
	v_lshl_add_u64 v[160:161], s[92:93], 0, v[130:131]
	s_mov_b32 m0, s33
	s_nop 0
	global_load_lds_dwordx4 v[160:161], off
	s_waitcnt lgkmcnt(8)
	s_barrier
	s_setprio 1
	s_waitcnt lgkmcnt(0)
	s_bitcmp1_b32 s100, 0
	s_cbranch_scc1 .Lg1p_skip1
	v_mfma_f32_16x16x32_f16 v[126:129], v[172:175], v[152:155], v[126:129]
	v_mfma_f32_16x16x32_f16 v[122:125], v[172:175], v[164:167], v[122:125]
	v_mfma_f32_16x16x32_f16 v[118:121], v[184:187], v[152:155], v[118:121]
	v_mfma_f32_16x16x32_f16 v[114:117], v[184:187], v[164:167], v[114:117]
	v_mfma_f32_16x16x32_f16 v[110:113], v[192:195], v[152:155], v[110:113]
	v_mfma_f32_16x16x32_f16 v[106:109], v[192:195], v[164:167], v[106:109]
	v_mfma_f32_16x16x32_f16 v[102:105], v[200:203], v[152:155], v[102:105]
	v_mfma_f32_16x16x32_f16 v[98:101], v[200:203], v[164:167], v[98:101]
	v_mfma_f32_16x16x32_f16 v[126:129], v[176:179], v[156:159], v[126:129]
	v_mfma_f32_16x16x32_f16 v[122:125], v[176:179], v[168:171], v[122:125]
	v_mfma_f32_16x16x32_f16 v[118:121], v[188:191], v[156:159], v[118:121]
	v_mfma_f32_16x16x32_f16 v[114:117], v[188:191], v[168:171], v[114:117]
	v_mfma_f32_16x16x32_f16 v[110:113], v[196:199], v[156:159], v[110:113]
	v_mfma_f32_16x16x32_f16 v[106:109], v[196:199], v[168:171], v[106:109]
	v_mfma_f32_16x16x32_f16 v[102:105], v[204:207], v[156:159], v[102:105]
	v_mfma_f32_16x16x32_f16 v[98:101], v[204:207], v[168:171], v[98:101]
.Lg1p_skip1:
	s_setprio 0
	s_barrier
	s_add_i32 s57, s84, 2
	s_lshl_b32 s82, s57, 7
	s_add_u32 s92, s4, s82
	s_addc_u32 s93, s5, 0
	s_mov_b32 m0, s53
	v_lshl_add_u64 v[160:161], s[92:93], 0, v[162:163]
	s_add_u32 s92, s92, 0x40000
	s_addc_u32 s93, s93, 0
	ds_read_b128 v[208:211], v150
	ds_read_b128 v[212:215], v150 offset:1024
	ds_read_b128 v[216:219], v150 offset:2048
	ds_read_b128 v[220:223], v150 offset:3072
	global_load_lds_dwordx4 v[160:161], off
	s_mov_b32 m0, s55
	v_lshl_add_u64 v[160:161], s[92:93], 0, v[162:163]
	global_load_lds_dwordx4 v[160:161], off
	s_barrier
	s_setprio 1
	s_waitcnt lgkmcnt(0)
	s_bitcmp1_b32 s100, 0
	s_cbranch_scc1 .Lg1p_skip2
	v_mfma_f32_16x16x32_f16 v[94:97], v[172:175], v[208:211], v[94:97]
	v_mfma_f32_16x16x32_f16 v[90:93], v[172:175], v[216:219], v[90:93]
	v_mfma_f32_16x16x32_f16 v[86:89], v[184:187], v[208:211], v[86:89]
	v_mfma_f32_16x16x32_f16 v[82:85], v[184:187], v[216:219], v[82:85]
	v_mfma_f32_16x16x32_f16 v[78:81], v[192:195], v[208:211], v[78:81]
	v_mfma_f32_16x16x32_f16 v[74:77], v[192:195], v[216:219], v[74:77]
	v_mfma_f32_16x16x32_f16 v[70:73], v[200:203], v[208:211], v[70:73]
	v_mfma_f32_16x16x32_f16 v[66:69], v[200:203], v[216:219], v[66:69]
	v_mfma_f32_16x16x32_f16 v[94:97], v[176:179], v[212:215], v[94:97]
	v_mfma_f32_16x16x32_f16 v[90:93], v[176:179], v[220:223], v[90:93]
	v_mfma_f32_16x16x32_f16 v[86:89], v[188:191], v[212:215], v[86:89]
	v_mfma_f32_16x16x32_f16 v[82:85], v[188:191], v[220:223], v[82:85]
	v_mfma_f32_16x16x32_f16 v[78:81], v[196:199], v[212:215], v[78:81]
	v_mfma_f32_16x16x32_f16 v[74:77], v[196:199], v[220:223], v[74:77]
	v_mfma_f32_16x16x32_f16 v[70:73], v[204:207], v[212:215], v[70:73]
	v_mfma_f32_16x16x32_f16 v[66:69], v[204:207], v[220:223], v[66:69]
.Lg1p_skip2:
	s_setprio 0
	s_add_u32 s92, s24, s82
	s_addc_u32 s93, s25, 0
	s_mov_b32 m0, s52
	s_barrier
	v_lshl_add_u64 v[160:161], s[92:93], 0, v[134:135]
	ds_read_b128 v[172:175], v147 offset:16384
	ds_read_b128 v[176:179], v147 offset:17408
	ds_read_b128 v[184:187], v146 offset:16384
	ds_read_b128 v[188:191], v146 offset:17408
	ds_read_b128 v[192:195], v145 offset:16384
	ds_read_b128 v[196:199], v145 offset:17408
	ds_read_b128 v[200:203], v144 offset:16384
	ds_read_b128 v[204:207], v144 offset:17408
	global_load_lds_dwordx4 v[160:161], off
	v_lshl_add_u64 v[160:161], s[92:93], 0, v[136:137]
	s_mov_b32 m0, s86
	s_nop 0
	global_load_lds_dwordx4 v[160:161], off
	s_barrier
	s_setprio 1
	s_waitcnt lgkmcnt(0)
	s_bitcmp1_b32 s100, 1
	s_cbranch_scc1 .Lg1p_skip3
	v_mfma_f32_16x16x32_f16 v[62:65], v[172:175], v[152:155], v[62:65]
	v_mfma_f32_16x16x32_f16 v[58:61], v[172:175], v[164:167], v[58:61]
	v_mfma_f32_16x16x32_f16 v[54:57], v[184:187], v[152:155], v[54:57]
	v_mfma_f32_16x16x32_f16 v[50:53], v[184:187], v[164:167], v[50:53]
	v_mfma_f32_16x16x32_f16 v[46:49], v[192:195], v[152:155], v[46:49]
	v_mfma_f32_16x16x32_f16 v[42:45], v[192:195], v[164:167], v[42:45]
	v_mfma_f32_16x16x32_f16 v[38:41], v[200:203], v[152:155], v[38:41]
	v_mfma_f32_16x16x32_f16 v[34:37], v[200:203], v[164:167], v[34:37]
	v_mfma_f32_16x16x32_f16 v[62:65], v[176:179], v[156:159], v[62:65]
	v_mfma_f32_16x16x32_f16 v[58:61], v[176:179], v[168:171], v[58:61]
	v_mfma_f32_16x16x32_f16 v[54:57], v[188:191], v[156:159], v[54:57]
	v_mfma_f32_16x16x32_f16 v[50:53], v[188:191], v[168:171], v[50:53]
	v_mfma_f32_16x16x32_f16 v[46:49], v[196:199], v[156:159], v[46:49]
	v_mfma_f32_16x16x32_f16 v[42:45], v[196:199], v[168:171], v[42:45]
	v_mfma_f32_16x16x32_f16 v[38:41], v[204:207], v[156:159], v[38:41]
	v_mfma_f32_16x16x32_f16 v[34:37], v[204:207], v[168:171], v[34:37]
.Lg1p_skip3:
	s_setprio 0
	s_barrier
	s_add_u32 s94, s10, s82
	s_addc_u32 s95, s11, 0
	s_mov_b32 m0, s87
	v_lshl_add_u64 v[152:153], s[94:95], 0, v[162:163]
	s_add_u32 s94, s94, 0x40000
	s_addc_u32 s95, s95, 0
	global_load_lds_dwordx4 v[152:153], off
	s_mov_b32 m0, s88
	v_lshl_add_u64 v[152:153], s[94:95], 0, v[162:163]
	global_load_lds_dwordx4 v[152:153], off
	s_waitcnt vmcnt(6)
	s_barrier
	s_setprio 1
	s_bitcmp1_b32 s100, 1
	s_cbranch_scc1 .Lg1p_skip4
	v_mfma_f32_16x16x32_f16 v[30:33], v[172:175], v[208:211], v[30:33]
	v_mfma_f32_16x16x32_f16 v[26:29], v[172:175], v[216:219], v[26:29]
	v_mfma_f32_16x16x32_f16 v[22:25], v[184:187], v[208:211], v[22:25]
	v_mfma_f32_16x16x32_f16 v[18:21], v[184:187], v[216:219], v[18:21]
	v_mfma_f32_16x16x32_f16 v[14:17], v[192:195], v[208:211], v[14:17]
	v_mfma_f32_16x16x32_f16 v[10:13], v[192:195], v[216:219], v[10:13]
	v_mfma_f32_16x16x32_f16 v[6:9], v[200:203], v[208:211], v[6:9]
	v_mfma_f32_16x16x32_f16 v[2:5], v[200:203], v[216:219], v[2:5]
	v_mfma_f32_16x16x32_f16 v[30:33], v[176:179], v[212:215], v[30:33]
	v_mfma_f32_16x16x32_f16 v[26:29], v[176:179], v[220:223], v[26:29]
	v_mfma_f32_16x16x32_f16 v[22:25], v[188:191], v[212:215], v[22:25]
	v_mfma_f32_16x16x32_f16 v[18:21], v[188:191], v[220:223], v[18:21]
	v_mfma_f32_16x16x32_f16 v[14:17], v[196:199], v[212:215], v[14:17]
	v_mfma_f32_16x16x32_f16 v[10:13], v[196:199], v[220:223], v[10:13]
	v_mfma_f32_16x16x32_f16 v[6:9], v[204:207], v[212:215], v[6:9]
	v_mfma_f32_16x16x32_f16 v[2:5], v[204:207], v[220:223], v[2:5]
.Lg1p_skip4:
	s_setprio 0
	s_barrier
	ds_read_b128 v[152:155], v149
	ds_read_b128 v[156:159], v149 offset:1024
	ds_read_b128 v[164:167], v149 offset:2048
	ds_read_b128 v[168:171], v149 offset:3072
	s_mov_b32 m0, s89
	v_lshl_add_u64 v[160:161], s[92:93], 0, v[132:133]
	ds_read_b128 v[172:175], v147 offset:32768
	ds_read_b128 v[176:179], v147 offset:33792
	ds_read_b128 v[184:187], v146 offset:32768
	ds_read_b128 v[188:191], v146 offset:33792
	ds_read_b128 v[192:195], v145 offset:32768
	ds_read_b128 v[196:199], v145 offset:33792
	ds_read_b128 v[200:203], v144 offset:32768
	ds_read_b128 v[204:207], v144 offset:33792
	global_load_lds_dwordx4 v[160:161], off
	v_lshl_add_u64 v[160:161], s[92:93], 0, v[130:131]
	s_mov_b32 m0, s90
	s_nop 0
	global_load_lds_dwordx4 v[160:161], off
	s_waitcnt lgkmcnt(8)
	s_barrier
	s_setprio 1
	s_waitcnt lgkmcnt(0)
	s_bitcmp1_b32 s100, 0
	s_cbranch_scc1 .Lg1p_skip5
	v_mfma_f32_16x16x32_f16 v[126:129], v[172:175], v[152:155], v[126:129]
	v_mfma_f32_16x16x32_f16 v[122:125], v[172:175], v[164:167], v[122:125]
	v_mfma_f32_16x16x32_f16 v[118:121], v[184:187], v[152:155], v[118:121]
	v_mfma_f32_16x16x32_f16 v[114:117], v[184:187], v[164:167], v[114:117]
	v_mfma_f32_16x16x32_f16 v[110:113], v[192:195], v[152:155], v[110:113]
	v_mfma_f32_16x16x32_f16 v[106:109], v[192:195], v[164:167], v[106:109]
	v_mfma_f32_16x16x32_f16 v[102:105], v[200:203], v[152:155], v[102:105]
	v_mfma_f32_16x16x32_f16 v[98:101], v[200:203], v[164:167], v[98:101]
	v_mfma_f32_16x16x32_f16 v[126:129], v[176:179], v[156:159], v[126:129]
	v_mfma_f32_16x16x32_f16 v[122:125], v[176:179], v[168:171], v[122:125]
	v_mfma_f32_16x16x32_f16 v[118:121], v[188:191], v[156:159], v[118:121]
	v_mfma_f32_16x16x32_f16 v[114:117], v[188:191], v[168:171], v[114:117]
	v_mfma_f32_16x16x32_f16 v[110:113], v[196:199], v[156:159], v[110:113]
	v_mfma_f32_16x16x32_f16 v[106:109], v[196:199], v[168:171], v[106:109]
	v_mfma_f32_16x16x32_f16 v[102:105], v[204:207], v[156:159], v[102:105]
	v_mfma_f32_16x16x32_f16 v[98:101], v[204:207], v[168:171], v[98:101]
.Lg1p_skip5:
	s_setprio 0
	s_barrier
	s_add_u32 s82, s4, s58
	s_addc_u32 s83, s5, 0
	s_add_u32 s92, s82, 0x180
	s_addc_u32 s93, s83, 0
	s_add_i32 m0, s52, 0x18000
	v_lshl_add_u64 v[160:161], s[92:93], 0, v[162:163]
	s_add_u32 s92, s92, 0x40000
	s_addc_u32 s93, s93, 0
	ds_read_b128 v[208:211], v148
	ds_read_b128 v[212:215], v148 offset:1024
	ds_read_b128 v[216:219], v148 offset:2048
	ds_read_b128 v[220:223], v148 offset:3072
	global_load_lds_dwordx4 v[160:161], off
	s_add_i32 m0, s52, 0x1a000
	v_lshl_add_u64 v[160:161], s[92:93], 0, v[162:163]
	global_load_lds_dwordx4 v[160:161], off
	s_barrier
	s_setprio 1
	s_waitcnt lgkmcnt(0)
	s_bitcmp1_b32 s100, 0
	s_cbranch_scc1 .Lg1p_skip6
	v_mfma_f32_16x16x32_f16 v[94:97], v[172:175], v[208:211], v[94:97]
	v_mfma_f32_16x16x32_f16 v[90:93], v[172:175], v[216:219], v[90:93]
	v_mfma_f32_16x16x32_f16 v[86:89], v[184:187], v[208:211], v[86:89]
	v_mfma_f32_16x16x32_f16 v[82:85], v[184:187], v[216:219], v[82:85]
	v_mfma_f32_16x16x32_f16 v[78:81], v[192:195], v[208:211], v[78:81]
	v_mfma_f32_16x16x32_f16 v[74:77], v[192:195], v[216:219], v[74:77]
	v_mfma_f32_16x16x32_f16 v[70:73], v[200:203], v[208:211], v[70:73]
	v_mfma_f32_16x16x32_f16 v[66:69], v[200:203], v[216:219], v[66:69]
	v_mfma_f32_16x16x32_f16 v[94:97], v[176:179], v[212:215], v[94:97]
	v_mfma_f32_16x16x32_f16 v[90:93], v[176:179], v[220:223], v[90:93]
	v_mfma_f32_16x16x32_f16 v[86:89], v[188:191], v[212:215], v[86:89]
	v_mfma_f32_16x16x32_f16 v[82:85], v[188:191], v[220:223], v[82:85]
	v_mfma_f32_16x16x32_f16 v[78:81], v[196:199], v[212:215], v[78:81]
	v_mfma_f32_16x16x32_f16 v[74:77], v[196:199], v[220:223], v[74:77]
	v_mfma_f32_16x16x32_f16 v[70:73], v[204:207], v[212:215], v[70:73]
	v_mfma_f32_16x16x32_f16 v[66:69], v[204:207], v[220:223], v[66:69]
.Lg1p_skip6:
	s_setprio 0
	s_add_u32 s92, s59, 0x180
	s_addc_u32 s93, s91, 0
	s_mov_b32 m0, s34
	s_barrier
	v_lshl_add_u64 v[160:161], s[92:93], 0, v[134:135]
	ds_read_b128 v[172:175], v147 offset:49152
	ds_read_b128 v[176:179], v147 offset:50176
	ds_read_b128 v[184:187], v146 offset:49152
	ds_read_b128 v[188:191], v146 offset:50176
	ds_read_b128 v[192:195], v145 offset:49152
	ds_read_b128 v[196:199], v145 offset:50176
	ds_read_b128 v[200:203], v144 offset:49152
	ds_read_b128 v[204:207], v144 offset:50176
	global_load_lds_dwordx4 v[160:161], off
	v_lshl_add_u64 v[160:161], s[92:93], 0, v[136:137]
	s_mov_b32 m0, s35
	s_nop 0
	global_load_lds_dwordx4 v[160:161], off
	s_barrier
	s_setprio 1
	s_waitcnt lgkmcnt(0)
	s_bitcmp1_b32 s100, 1
	s_cbranch_scc1 .Lg1p_skip7
	v_mfma_f32_16x16x32_f16 v[62:65], v[172:175], v[152:155], v[62:65]
	v_mfma_f32_16x16x32_f16 v[58:61], v[172:175], v[164:167], v[58:61]
	v_mfma_f32_16x16x32_f16 v[54:57], v[184:187], v[152:155], v[54:57]
	v_mfma_f32_16x16x32_f16 v[50:53], v[184:187], v[164:167], v[50:53]
	v_mfma_f32_16x16x32_f16 v[46:49], v[192:195], v[152:155], v[46:49]
	v_mfma_f32_16x16x32_f16 v[42:45], v[192:195], v[164:167], v[42:45]
	v_mfma_f32_16x16x32_f16 v[38:41], v[200:203], v[152:155], v[38:41]
	v_mfma_f32_16x16x32_f16 v[34:37], v[200:203], v[164:167], v[34:37]
	v_mfma_f32_16x16x32_f16 v[62:65], v[176:179], v[156:159], v[62:65]
	v_mfma_f32_16x16x32_f16 v[58:61], v[176:179], v[168:171], v[58:61]
	v_mfma_f32_16x16x32_f16 v[54:57], v[188:191], v[156:159], v[54:57]
	v_mfma_f32_16x16x32_f16 v[50:53], v[188:191], v[168:171], v[50:53]
	v_mfma_f32_16x16x32_f16 v[46:49], v[196:199], v[156:159], v[46:49]
	v_mfma_f32_16x16x32_f16 v[42:45], v[196:199], v[168:171], v[42:45]
	v_mfma_f32_16x16x32_f16 v[38:41], v[204:207], v[156:159], v[38:41]
	v_mfma_f32_16x16x32_f16 v[34:37], v[204:207], v[168:171], v[34:37]
.Lg1p_skip7:
	s_setprio 0
	s_barrier
	s_add_u32 s58, s10, s58
	s_addc_u32 s59, s11, 0
	s_add_u32 s58, s58, 0x180
	s_addc_u32 s59, s59, 0
	s_add_i32 m0, s52, 0x1c000
	v_lshl_add_u64 v[152:153], s[58:59], 0, v[162:163]
	s_add_u32 s58, s58, 0x40000
	s_addc_u32 s59, s59, 0
	global_load_lds_dwordx4 v[152:153], off
	s_add_i32 m0, s52, 0x1e000
	v_lshl_add_u64 v[152:153], s[58:59], 0, v[162:163]
	global_load_lds_dwordx4 v[152:153], off
	s_waitcnt vmcnt(6)
	s_barrier
	s_setprio 1
	s_bitcmp1_b32 s100, 1
	s_cbranch_scc1 .Lg1p_skip8
	v_mfma_f32_16x16x32_f16 v[30:33], v[172:175], v[208:211], v[30:33]
	v_mfma_f32_16x16x32_f16 v[26:29], v[172:175], v[216:219], v[26:29]
	v_mfma_f32_16x16x32_f16 v[22:25], v[184:187], v[208:211], v[22:25]
	v_mfma_f32_16x16x32_f16 v[18:21], v[184:187], v[216:219], v[18:21]
	v_mfma_f32_16x16x32_f16 v[14:17], v[192:195], v[208:211], v[14:17]
	v_mfma_f32_16x16x32_f16 v[10:13], v[192:195], v[216:219], v[10:13]
	v_mfma_f32_16x16x32_f16 v[6:9], v[200:203], v[208:211], v[6:9]
	v_mfma_f32_16x16x32_f16 v[2:5], v[200:203], v[216:219], v[2:5]
	v_mfma_f32_16x16x32_f16 v[30:33], v[176:179], v[212:215], v[30:33]
	v_mfma_f32_16x16x32_f16 v[26:29], v[176:179], v[220:223], v[26:29]
	v_mfma_f32_16x16x32_f16 v[22:25], v[188:191], v[212:215], v[22:25]
	v_mfma_f32_16x16x32_f16 v[18:21], v[188:191], v[220:223], v[18:21]
	v_mfma_f32_16x16x32_f16 v[14:17], v[196:199], v[212:215], v[14:17]
	v_mfma_f32_16x16x32_f16 v[10:13], v[196:199], v[220:223], v[10:13]
	v_mfma_f32_16x16x32_f16 v[6:9], v[204:207], v[212:215], v[6:9]
	v_mfma_f32_16x16x32_f16 v[2:5], v[204:207], v[220:223], v[2:5]
.Lg1p_skip8:
	s_setprio 0
	s_cmp_lt_u32 s84, 28
	s_mov_b32 s84, s57
	s_barrier
	s_cbranch_scc1 .Lg1p_loop
	v_readlane_b32 s4, v244, 8
	v_readlane_b32 s5, v244, 9
	s_mov_b32 m0, s56
	ds_read_b128 v[134:137], v151
	ds_read_b128 v[152:155], v151 offset:1024
	ds_read_b128 v[156:159], v151 offset:2048
	ds_read_b128 v[164:167], v151 offset:3072
	ds_read_b128 v[168:171], v147
	ds_read_b128 v[172:175], v147 offset:1024
	ds_read_b128 v[176:179], v146
	ds_read_b128 v[184:187], v146 offset:1024
	ds_read_b128 v[188:191], v145
	ds_read_b128 v[192:195], v145 offset:1024
	ds_read_b128 v[196:199], v144
	ds_read_b128 v[200:203], v144 offset:1024
	v_lshl_add_u64 v[132:133], s[4:5], 0, v[132:133]
	global_load_lds_dwordx4 v[132:133], off
	v_lshl_add_u64 v[130:131], s[4:5], 0, v[130:131]
	s_mov_b32 m0, s33
	s_nop 0
	global_load_lds_dwordx4 v[130:131], off
	s_barrier
	s_setprio 1
	s_waitcnt lgkmcnt(0)
	s_bitcmp1_b32 s100, 0
	s_cbranch_scc1 .Lg1p_skip9
	v_mfma_f32_16x16x32_f16 v[126:129], v[168:171], v[134:137], v[126:129]
	v_mfma_f32_16x16x32_f16 v[122:125], v[168:171], v[156:159], v[122:125]
	v_mfma_f32_16x16x32_f16 v[110:113], v[188:191], v[134:137], v[110:113]
	v_mfma_f32_16x16x32_f16 v[106:109], v[188:191], v[156:159], v[106:109]
	v_mfma_f32_16x16x32_f16 v[126:129], v[172:175], v[152:155], v[126:129]
	v_mfma_f32_16x16x32_f16 v[122:125], v[172:175], v[164:167], v[122:125]
	v_mfma_f32_16x16x32_f16 v[118:121], v[176:179], v[134:137], v[118:121]
	v_mfma_f32_16x16x32_f16 v[114:117], v[176:179], v[156:159], v[114:117]
	v_mfma_f32_16x16x32_f16 v[110:113], v[192:195], v[152:155], v[110:113]
	v_mfma_f32_16x16x32_f16 v[106:109], v[192:195], v[164:167], v[106:109]
	v_mfma_f32_16x16x32_f16 v[102:105], v[196:199], v[134:137], v[102:105]
	v_mfma_f32_16x16x32_f16 v[98:101], v[196:199], v[156:159], v[98:101]
	v_mfma_f32_16x16x32_f16 v[130:133], v[184:187], v[152:155], v[118:121]
	v_mfma_f32_16x16x32_f16 v[204:207], v[184:187], v[164:167], v[114:117]
	v_mfma_f32_16x16x32_f16 v[208:211], v[200:203], v[152:155], v[102:105]
	v_mfma_f32_16x16x32_f16 v[212:215], v[200:203], v[164:167], v[98:101]
.Lg1p_skip9:
	s_setprio 0
	s_barrier
	s_nop 1
	ds_read_b128 v[98:101], v150
	ds_read_b128 v[102:105], v150 offset:1024
	ds_read_b128 v[114:117], v150 offset:2048
	ds_read_b128 v[118:121], v150 offset:3072
	s_barrier
	s_setprio 1
	s_waitcnt lgkmcnt(0)
	s_bitcmp1_b32 s100, 0
	s_cbranch_scc1 .Lg1p_skip10
	v_mfma_f32_16x16x32_f16 v[94:97], v[168:171], v[98:101], v[94:97]
	v_mfma_f32_16x16x32_f16 v[90:93], v[168:171], v[114:117], v[90:93]
	v_mfma_f32_16x16x32_f16 v[78:81], v[188:191], v[98:101], v[78:81]
	v_mfma_f32_16x16x32_f16 v[74:77], v[188:191], v[114:117], v[74:77]
	v_mfma_f32_16x16x32_f16 v[94:97], v[172:175], v[102:105], v[94:97]
	v_mfma_f32_16x16x32_f16 v[90:93], v[172:175], v[118:121], v[90:93]
	v_mfma_f32_16x16x32_f16 v[86:89], v[176:179], v[98:101], v[86:89]
	v_mfma_f32_16x16x32_f16 v[82:85], v[176:179], v[114:117], v[82:85]
	v_mfma_f32_16x16x32_f16 v[78:81], v[192:195], v[102:105], v[78:81]
	v_mfma_f32_16x16x32_f16 v[74:77], v[192:195], v[118:121], v[74:77]
	v_mfma_f32_16x16x32_f16 v[70:73], v[196:199], v[98:101], v[70:73]
	v_mfma_f32_16x16x32_f16 v[66:69], v[196:199], v[114:117], v[66:69]
	v_mfma_f32_16x16x32_f16 v[168:171], v[184:187], v[102:105], v[86:89]
	v_mfma_f32_16x16x32_f16 v[172:175], v[184:187], v[118:121], v[82:85]
	v_mfma_f32_16x16x32_f16 v[176:179], v[200:203], v[102:105], v[70:73]
	v_mfma_f32_16x16x32_f16 v[184:187], v[200:203], v[118:121], v[66:69]
.Lg1p_skip10:
	s_setprio 0
	s_barrier
	s_nop 1
	ds_read_b128 v[66:69], v147 offset:16384
	ds_read_b128 v[70:73], v147 offset:17408
	ds_read_b128 v[82:85], v146 offset:16384
	ds_read_b128 v[86:89], v146 offset:17408
	ds_read_b128 v[188:191], v145 offset:16384
	ds_read_b128 v[192:195], v145 offset:17408
	ds_read_b128 v[196:199], v144 offset:16384
	ds_read_b128 v[200:203], v144 offset:17408
	s_waitcnt vmcnt(4)
	s_barrier
	s_setprio 1
	s_waitcnt lgkmcnt(0)
	s_bitcmp1_b32 s100, 1
	s_cbranch_scc1 .Lg1p_skip11
	v_mfma_f32_16x16x32_f16 v[62:65], v[66:69], v[134:137], v[62:65]
	v_mfma_f32_16x16x32_f16 v[58:61], v[66:69], v[156:159], v[58:61]
	v_mfma_f32_16x16x32_f16 v[46:49], v[188:191], v[134:137], v[46:49]
	v_mfma_f32_16x16x32_f16 v[42:45], v[188:191], v[156:159], v[42:45]
	v_mfma_f32_16x16x32_f16 v[62:65], v[70:73], v[152:155], v[62:65]
	v_mfma_f32_16x16x32_f16 v[58:61], v[70:73], v[164:167], v[58:61]
	v_mfma_f32_16x16x32_f16 v[54:57], v[82:85], v[134:137], v[54:57]
	v_mfma_f32_16x16x32_f16 v[50:53], v[82:85], v[156:159], v[50:53]
	v_mfma_f32_16x16x32_f16 v[46:49], v[192:195], v[152:155], v[46:49]
	v_mfma_f32_16x16x32_f16 v[42:45], v[192:195], v[164:167], v[42:45]
	v_mfma_f32_16x16x32_f16 v[38:41], v[196:199], v[134:137], v[38:41]
	v_mfma_f32_16x16x32_f16 v[34:37], v[196:199], v[156:159], v[34:37]
	v_mfma_f32_16x16x32_f16 v[216:219], v[86:89], v[152:155], v[54:57]
	v_mfma_f32_16x16x32_f16 v[220:223], v[86:89], v[164:167], v[50:53]
	v_mfma_f32_16x16x32_f16 v[134:137], v[200:203], v[152:155], v[38:41]
	v_mfma_f32_16x16x32_f16 v[150:153], v[200:203], v[164:167], v[34:37]
.Lg1p_skip11:
	s_setprio 0
	s_setprio 1
	s_bitcmp1_b32 s100, 1
	s_cbranch_scc1 .Lg1p_skip12
	v_mfma_f32_16x16x32_f16 v[30:33], v[66:69], v[98:101], v[30:33]
	v_mfma_f32_16x16x32_f16 v[26:29], v[66:69], v[114:117], v[26:29]
	v_mfma_f32_16x16x32_f16 v[14:17], v[188:191], v[98:101], v[14:17]
	v_mfma_f32_16x16x32_f16 v[10:13], v[188:191], v[114:117], v[10:13]
	v_mfma_f32_16x16x32_f16 v[30:33], v[70:73], v[102:105], v[30:33]
	v_mfma_f32_16x16x32_f16 v[26:29], v[70:73], v[118:121], v[26:29]
	v_mfma_f32_16x16x32_f16 v[22:25], v[82:85], v[98:101], v[22:25]
	v_mfma_f32_16x16x32_f16 v[18:21], v[82:85], v[114:117], v[18:21]
	v_mfma_f32_16x16x32_f16 v[14:17], v[192:195], v[102:105], v[14:17]
	v_mfma_f32_16x16x32_f16 v[10:13], v[192:195], v[118:121], v[10:13]
	v_mfma_f32_16x16x32_f16 v[6:9], v[196:199], v[98:101], v[6:9]
	v_mfma_f32_16x16x32_f16 v[2:5], v[196:199], v[114:117], v[2:5]
	v_mfma_f32_16x16x32_f16 v[154:157], v[86:89], v[102:105], v[22:25]
	v_mfma_f32_16x16x32_f16 v[158:161], v[86:89], v[118:121], v[18:21]
	v_mfma_f32_16x16x32_f16 v[164:167], v[200:203], v[102:105], v[6:9]
	v_mfma_f32_16x16x32_f16 v[188:191], v[200:203], v[118:121], v[2:5]
.Lg1p_skip12:
	s_setprio 0
	s_barrier
	s_nop 1
	ds_read_b128 v[2:5], v149
	ds_read_b128 v[6:9], v149 offset:1024
	ds_read_b128 v[192:195], v149 offset:2048
	ds_read_b128 v[196:199], v149 offset:3072
	ds_read_b128 v[18:21], v147 offset:32768
	ds_read_b128 v[22:25], v147 offset:33792
	ds_read_b128 v[34:37], v146 offset:32768
	ds_read_b128 v[38:41], v146 offset:33792
	ds_read_b128 v[50:53], v145 offset:32768
	ds_read_b128 v[54:57], v145 offset:33792
	ds_read_b128 v[200:203], v144 offset:32768
	ds_read_b128 v[224:227], v144 offset:33792
	s_waitcnt vmcnt(2)
	s_barrier
	s_setprio 1
	s_waitcnt lgkmcnt(0)
	s_bitcmp1_b32 s100, 0
	s_cbranch_scc1 .Lg1p_skip13
	v_mfma_f32_16x16x32_f16 v[66:69], v[18:21], v[2:5], v[126:129]
	v_mfma_f32_16x16x32_f16 v[118:121], v[22:25], v[6:9], v[66:69]
	v_mfma_f32_16x16x32_f16 v[66:69], v[18:21], v[192:195], v[122:125]
	v_mfma_f32_16x16x32_f16 v[114:117], v[22:25], v[196:199], v[66:69]
	v_mfma_f32_16x16x32_f16 v[66:69], v[34:37], v[2:5], v[130:133]
	v_mfma_f32_16x16x32_f16 v[102:105], v[38:41], v[6:9], v[66:69]
	v_mfma_f32_16x16x32_f16 v[66:69], v[34:37], v[192:195], v[204:207]
	v_mfma_f32_16x16x32_f16 v[98:101], v[38:41], v[196:199], v[66:69]
	v_mfma_f32_16x16x32_f16 v[66:69], v[50:53], v[2:5], v[110:113]
	v_mfma_f32_16x16x32_f16 v[86:89], v[54:57], v[6:9], v[66:69]
	v_mfma_f32_16x16x32_f16 v[66:69], v[50:53], v[192:195], v[106:109]
	v_mfma_f32_16x16x32_f16 v[82:85], v[54:57], v[196:199], v[66:69]
	v_mfma_f32_16x16x32_f16 v[66:69], v[200:203], v[2:5], v[208:211]
	v_mfma_f32_16x16x32_f16 v[70:73], v[224:227], v[6:9], v[66:69]
	v_mfma_f32_16x16x32_f16 v[66:69], v[200:203], v[192:195], v[212:215]
	v_mfma_f32_16x16x32_f16 v[66:69], v[224:227], v[196:199], v[66:69]
.Lg1p_skip13:
	s_setprio 0
	s_barrier
	ds_read_b128 v[130:133], v148
	ds_read_b128 v[204:207], v148 offset:1024
	ds_read_b128 v[208:211], v148 offset:2048
	ds_read_b128 v[212:215], v148 offset:3072
	s_waitcnt vmcnt(0)
	s_barrier
	s_setprio 1
	s_waitcnt lgkmcnt(0)
	s_bitcmp1_b32 s100, 0
	s_cbranch_scc1 .Lg1p_skip14
	v_mfma_f32_16x16x32_f16 v[94:97], v[18:21], v[130:133], v[94:97]
	v_mfma_f32_16x16x32_f16 v[18:21], v[18:21], v[208:211], v[90:93]
	v_mfma_f32_16x16x32_f16 v[122:125], v[22:25], v[212:215], v[18:21]
	v_mfma_f32_16x16x32_f16 v[18:21], v[34:37], v[130:133], v[168:171]
	v_mfma_f32_16x16x32_f16 v[110:113], v[38:41], v[204:207], v[18:21]
	v_mfma_f32_16x16x32_f16 v[18:21], v[34:37], v[208:211], v[172:175]
	v_mfma_f32_16x16x32_f16 v[106:109], v[38:41], v[212:215], v[18:21]
	v_mfma_f32_16x16x32_f16 v[18:21], v[50:53], v[130:133], v[78:81]
	v_mfma_f32_16x16x32_f16 v[126:129], v[22:25], v[204:207], v[94:97]
	v_mfma_f32_16x16x32_f16 v[94:97], v[54:57], v[204:207], v[18:21]
	v_mfma_f32_16x16x32_f16 v[18:21], v[50:53], v[208:211], v[74:77]
	v_mfma_f32_16x16x32_f16 v[90:93], v[54:57], v[212:215], v[18:21]
	v_mfma_f32_16x16x32_f16 v[18:21], v[200:203], v[130:133], v[176:179]
	v_mfma_f32_16x16x32_f16 v[78:81], v[224:227], v[204:207], v[18:21]
	v_mfma_f32_16x16x32_f16 v[18:21], v[200:203], v[208:211], v[184:187]
	v_mfma_f32_16x16x32_f16 v[74:77], v[224:227], v[212:215], v[18:21]
.Lg1p_skip14:
	s_setprio 0
	s_barrier
	ds_read_b128 v[168:171], v147 offset:49152
	ds_read_b128 v[172:175], v147 offset:50176
	ds_read_b128 v[176:179], v146 offset:49152
	ds_read_b128 v[146:149], v146 offset:50176
	ds_read_b128 v[184:187], v145 offset:49152
	ds_read_b128 v[200:203], v145 offset:50176
	ds_read_b128 v[224:227], v144 offset:49152
	ds_read_b128 v[228:231], v144 offset:50176
	s_barrier
	s_setprio 1
	s_waitcnt lgkmcnt(0)
	s_bitcmp1_b32 s100, 1
	s_cbranch_scc1 .Lg1p_skip15
	v_mfma_f32_16x16x32_f16 v[18:21], v[168:171], v[2:5], v[62:65]
	v_mfma_f32_16x16x32_f16 v[54:57], v[172:175], v[6:9], v[18:21]
	v_mfma_f32_16x16x32_f16 v[18:21], v[168:171], v[192:195], v[58:61]
	v_mfma_f32_16x16x32_f16 v[50:53], v[172:175], v[196:199], v[18:21]
	v_mfma_f32_16x16x32_f16 v[18:21], v[176:179], v[2:5], v[216:219]
	v_mfma_f32_16x16x32_f16 v[38:41], v[146:149], v[6:9], v[18:21]
	v_mfma_f32_16x16x32_f16 v[18:21], v[176:179], v[192:195], v[220:223]
	v_mfma_f32_16x16x32_f16 v[34:37], v[146:149], v[196:199], v[18:21]
	v_mfma_f32_16x16x32_f16 v[18:21], v[184:187], v[2:5], v[46:49]
	v_mfma_f32_16x16x32_f16 v[2:5], v[224:227], v[2:5], v[134:137]
	v_mfma_f32_16x16x32_f16 v[22:25], v[200:203], v[6:9], v[18:21]
	v_mfma_f32_16x16x32_f16 v[18:21], v[184:187], v[192:195], v[42:45]
	v_mfma_f32_16x16x32_f16 v[6:9], v[228:231], v[6:9], v[2:5]
	v_mfma_f32_16x16x32_f16 v[2:5], v[224:227], v[192:195], v[150:153]
	v_mfma_f32_16x16x32_f16 v[18:21], v[200:203], v[196:199], v[18:21]
	v_mfma_f32_16x16x32_f16 v[2:5], v[228:231], v[196:199], v[2:5]
.Lg1p_skip15:
	s_setprio 0
	s_setprio 1
	s_bitcmp1_b32 s100, 1
	s_cbranch_scc1 .Lg1p_skip16
	v_mfma_f32_16x16x32_f16 v[26:29], v[168:171], v[208:211], v[26:29]
	v_mfma_f32_16x16x32_f16 v[58:61], v[172:175], v[212:215], v[26:29]
	v_mfma_f32_16x16x32_f16 v[26:29], v[176:179], v[130:133], v[154:157]
	v_mfma_f32_16x16x32_f16 v[46:49], v[146:149], v[204:207], v[26:29]
	v_mfma_f32_16x16x32_f16 v[26:29], v[176:179], v[208:211], v[158:161]
	v_mfma_f32_16x16x32_f16 v[10:13], v[184:187], v[208:211], v[10:13]
	v_mfma_f32_16x16x32_f16 v[30:33], v[168:171], v[130:133], v[30:33]
	v_mfma_f32_16x16x32_f16 v[42:45], v[146:149], v[212:215], v[26:29]
	v_mfma_f32_16x16x32_f16 v[14:17], v[184:187], v[130:133], v[14:17]
	v_mfma_f32_16x16x32_f16 v[26:29], v[200:203], v[212:215], v[10:13]
	v_mfma_f32_16x16x32_f16 v[10:13], v[224:227], v[130:133], v[164:167]
	v_mfma_f32_16x16x32_f16 v[62:65], v[172:175], v[204:207], v[30:33]
	v_mfma_f32_16x16x32_f16 v[30:33], v[200:203], v[204:207], v[14:17]
	v_mfma_f32_16x16x32_f16 v[14:17], v[228:231], v[204:207], v[10:13]
	v_mfma_f32_16x16x32_f16 v[10:13], v[224:227], v[208:211], v[188:191]
	v_mfma_f32_16x16x32_f16 v[10:13], v[228:231], v[212:215], v[10:13]
.Lg1p_skip16:
	s_setprio 0
	s_branch .Lg1_join
.Lg2p_loop:
	ds_read_b128 v[140:143], v138
	ds_read_b128 v[154:157], v138 offset:1024
	ds_read_b128 v[158:161], v138 offset:2048
	ds_read_b128 v[164:167], v138 offset:3072
	s_lshl_b32 vcc_hi, s57, 7
	s_add_u32 s58, s88, vcc_hi
	s_addc_u32 s59, s89, 0
	s_add_u32 s82, s58, 0x80
	s_addc_u32 s83, s59, 0
	s_add_i32 s59, s97, 0xc000
	v_lshl_add_u64 v[144:145], s[82:83], 0, v[162:163]
	s_add_u32 s82, s82, 0x20000
	s_mov_b32 m0, s59
	s_addc_u32 s83, s83, 0
	s_add_i32 s58, s97, 0xe000
	ds_read_b128 v[168:171], v134
	ds_read_b128 v[172:175], v134 offset:1024
	ds_read_b128 v[176:179], v133
	ds_read_b128 v[184:187], v133 offset:1024
	ds_read_b128 v[188:191], v131
	ds_read_b128 v[192:195], v131 offset:1024
	ds_read_b128 v[196:199], v130
	ds_read_b128 v[200:203], v130 offset:1024
	global_load_lds_dwordx4 v[144:145], off
	s_mov_b32 m0, s58
	v_lshl_add_u64 v[144:145], s[82:83], 0, v[162:163]
	global_load_lds_dwordx4 v[144:145], off
	s_waitcnt lgkmcnt(8)
	s_barrier
	s_setprio 1
	s_waitcnt lgkmcnt(0)
	s_bitcmp1_b32 s100, 0
	s_cbranch_scc1 .Lg2p_skip1
	v_mfma_f32_16x16x32_f16 v[102:105], v[168:171], v[140:143], v[102:105]
	v_mfma_f32_16x16x32_f16 v[98:101], v[168:171], v[158:161], v[98:101]
	v_mfma_f32_16x16x32_f16 v[126:129], v[176:179], v[140:143], v[126:129]
	v_mfma_f32_16x16x32_f16 v[122:125], v[176:179], v[158:161], v[122:125]
	v_mfma_f32_16x16x32_f16 v[118:121], v[188:191], v[140:143], v[118:121]
	v_mfma_f32_16x16x32_f16 v[114:117], v[188:191], v[158:161], v[114:117]
	v_mfma_f32_16x16x32_f16 v[110:113], v[196:199], v[140:143], v[110:113]
	v_mfma_f32_16x16x32_f16 v[106:109], v[196:199], v[158:161], v[106:109]
	v_mfma_f32_16x16x32_f16 v[102:105], v[172:175], v[154:157], v[102:105]
	v_mfma_f32_16x16x32_f16 v[98:101], v[172:175], v[164:167], v[98:101]
	v_mfma_f32_16x16x32_f16 v[126:129], v[184:187], v[154:157], v[126:129]
	v_mfma_f32_16x16x32_f16 v[122:125], v[184:187], v[164:167], v[122:125]
	v_mfma_f32_16x16x32_f16 v[118:121], v[192:195], v[154:157], v[118:121]
	v_mfma_f32_16x16x32_f16 v[114:117], v[192:195], v[164:167], v[114:117]
	v_mfma_f32_16x16x32_f16 v[110:113], v[200:203], v[154:157], v[110:113]
	v_mfma_f32_16x16x32_f16 v[106:109], v[200:203], v[164:167], v[106:109]
.Lg2p_skip1:
	s_setprio 0
	s_barrier
	s_add_i32 vcc_lo, s57, 2
	s_lshl_b32 s78, vcc_lo, 7
	s_add_u32 s82, s92, s78
	s_addc_u32 s83, s93, 0
	s_mov_b32 m0, s84
	v_lshl_add_u64 v[144:145], s[82:83], 0, v[162:163]
	s_add_u32 s82, s82, 0x20000
	s_addc_u32 s83, s83, 0
	ds_read_b128 v[204:207], v137
	ds_read_b128 v[208:211], v137 offset:1024
	ds_read_b128 v[212:215], v137 offset:2048
	ds_read_b128 v[216:219], v137 offset:3072
	global_load_lds_dwordx4 v[144:145], off
	s_mov_b32 m0, s94
	v_lshl_add_u64 v[144:145], s[82:83], 0, v[162:163]
	global_load_lds_dwordx4 v[144:145], off
	s_barrier
	s_setprio 1
	s_waitcnt lgkmcnt(0)
	s_bitcmp1_b32 s100, 0
	s_cbranch_scc1 .Lg2p_skip2
	v_mfma_f32_16x16x32_f16 v[94:97], v[168:171], v[204:207], v[94:97]
	v_mfma_f32_16x16x32_f16 v[90:93], v[168:171], v[212:215], v[90:93]
	v_mfma_f32_16x16x32_f16 v[86:89], v[176:179], v[204:207], v[86:89]
	v_mfma_f32_16x16x32_f16 v[82:85], v[176:179], v[212:215], v[82:85]
	v_mfma_f32_16x16x32_f16 v[78:81], v[188:191], v[204:207], v[78:81]
	v_mfma_f32_16x16x32_f16 v[74:77], v[188:191], v[212:215], v[74:77]
	v_mfma_f32_16x16x32_f16 v[70:73], v[196:199], v[204:207], v[70:73]
	v_mfma_f32_16x16x32_f16 v[66:69], v[196:199], v[212:215], v[66:69]
	v_mfma_f32_16x16x32_f16 v[94:97], v[172:175], v[208:211], v[94:97]
	v_mfma_f32_16x16x32_f16 v[90:93], v[172:175], v[216:219], v[90:93]
	v_mfma_f32_16x16x32_f16 v[86:89], v[184:187], v[208:211], v[86:89]
	v_mfma_f32_16x16x32_f16 v[82:85], v[184:187], v[216:219], v[82:85]
	v_mfma_f32_16x16x32_f16 v[78:81], v[192:195], v[208:211], v[78:81]
	v_mfma_f32_16x16x32_f16 v[74:77], v[192:195], v[216:219], v[74:77]
	v_mfma_f32_16x16x32_f16 v[70:73], v[200:203], v[208:211], v[70:73]
	v_mfma_f32_16x16x32_f16 v[66:69], v[200:203], v[216:219], v[66:69]
.Lg2p_skip2:
	s_setprio 0
	s_add_u32 s82, s90, s78
	s_addc_u32 s83, s91, 0
	s_mov_b32 m0, s97
	v_lshl_add_u64 v[144:145], s[82:83], 0, v[162:163]
	s_add_u32 s82, s82, 0x20000
	s_addc_u32 s83, s83, 0
	s_barrier
	ds_read_b128 v[168:171], v134 offset:16384
	ds_read_b128 v[172:175], v134 offset:17408
	ds_read_b128 v[176:179], v133 offset:16384
	ds_read_b128 v[184:187], v133 offset:17408
	ds_read_b128 v[188:191], v131 offset:16384
	ds_read_b128 v[192:195], v131 offset:17408
	ds_read_b128 v[196:199], v130 offset:16384
	ds_read_b128 v[200:203], v130 offset:17408
	global_load_lds_dwordx4 v[144:145], off
	s_mov_b32 m0, s99
	v_lshl_add_u64 v[144:145], s[82:83], 0, v[162:163]
	global_load_lds_dwordx4 v[144:145], off
	s_barrier
	s_setprio 1
	s_waitcnt lgkmcnt(0)
	s_bitcmp1_b32 s100, 1
	s_cbranch_scc1 .Lg2p_skip3
	v_mfma_f32_16x16x32_f16 v[62:65], v[168:171], v[140:143], v[62:65]
	v_mfma_f32_16x16x32_f16 v[58:61], v[168:171], v[158:161], v[58:61]
	v_mfma_f32_16x16x32_f16 v[54:57], v[176:179], v[140:143], v[54:57]
	v_mfma_f32_16x16x32_f16 v[50:53], v[176:179], v[158:161], v[50:53]
	v_mfma_f32_16x16x32_f16 v[46:49], v[188:191], v[140:143], v[46:49]
	v_mfma_f32_16x16x32_f16 v[42:45], v[188:191], v[158:161], v[42:45]
	v_mfma_f32_16x16x32_f16 v[38:41], v[196:199], v[140:143], v[38:41]
	v_mfma_f32_16x16x32_f16 v[30:33], v[196:199], v[158:161], v[30:33]
	v_mfma_f32_16x16x32_f16 v[62:65], v[172:175], v[154:157], v[62:65]
	v_mfma_f32_16x16x32_f16 v[58:61], v[172:175], v[164:167], v[58:61]
	v_mfma_f32_16x16x32_f16 v[54:57], v[184:187], v[154:157], v[54:57]
	v_mfma_f32_16x16x32_f16 v[50:53], v[184:187], v[164:167], v[50:53]
	v_mfma_f32_16x16x32_f16 v[46:49], v[192:195], v[154:157], v[46:49]
	v_mfma_f32_16x16x32_f16 v[42:45], v[192:195], v[164:167], v[42:45]
	v_mfma_f32_16x16x32_f16 v[38:41], v[200:203], v[154:157], v[38:41]
	v_mfma_f32_16x16x32_f16 v[30:33], v[200:203], v[164:167], v[30:33]
.Lg2p_skip3:
	s_setprio 0
	s_barrier
	s_add_u32 s82, s34, s78
	s_addc_u32 s83, s35, 0
	s_mov_b32 m0, s95
	v_lshl_add_u64 v[140:141], s[82:83], 0, v[162:163]
	s_add_u32 s82, s82, 0x20000
	s_addc_u32 s83, s83, 0
	global_load_lds_dwordx4 v[140:141], off
	s_mov_b32 m0, s33
	v_lshl_add_u64 v[140:141], s[82:83], 0, v[162:163]
	global_load_lds_dwordx4 v[140:141], off
	s_waitcnt vmcnt(6)
	s_barrier
	s_setprio 1
	s_bitcmp1_b32 s100, 1
	s_cbranch_scc1 .Lg2p_skip4
	v_mfma_f32_16x16x32_f16 v[34:37], v[168:171], v[204:207], v[34:37]
	v_mfma_f32_16x16x32_f16 v[26:29], v[168:171], v[212:215], v[26:29]
	v_mfma_f32_16x16x32_f16 v[22:25], v[176:179], v[204:207], v[22:25]
	v_mfma_f32_16x16x32_f16 v[18:21], v[176:179], v[212:215], v[18:21]
	v_mfma_f32_16x16x32_f16 v[14:17], v[188:191], v[204:207], v[14:17]
	v_mfma_f32_16x16x32_f16 v[10:13], v[188:191], v[212:215], v[10:13]
	v_mfma_f32_16x16x32_f16 v[6:9], v[196:199], v[204:207], v[6:9]
	v_mfma_f32_16x16x32_f16 v[2:5], v[196:199], v[212:215], v[2:5]
	v_mfma_f32_16x16x32_f16 v[34:37], v[172:175], v[208:211], v[34:37]
	v_mfma_f32_16x16x32_f16 v[26:29], v[172:175], v[216:219], v[26:29]
	v_mfma_f32_16x16x32_f16 v[22:25], v[184:187], v[208:211], v[22:25]
	v_mfma_f32_16x16x32_f16 v[18:21], v[184:187], v[216:219], v[18:21]
	v_mfma_f32_16x16x32_f16 v[14:17], v[192:195], v[208:211], v[14:17]
	v_mfma_f32_16x16x32_f16 v[10:13], v[192:195], v[216:219], v[10:13]
	v_mfma_f32_16x16x32_f16 v[6:9], v[200:203], v[208:211], v[6:9]
	v_mfma_f32_16x16x32_f16 v[2:5], v[200:203], v[216:219], v[2:5]
.Lg2p_skip4:
	s_setprio 0
	s_barrier
	ds_read_b128 v[140:143], v136
	ds_read_b128 v[154:157], v136 offset:1024
	ds_read_b128 v[158:161], v136 offset:2048
	ds_read_b128 v[164:167], v136 offset:3072
	s_add_u32 s82, s88, s78
	s_addc_u32 s83, s89, 0
	s_mov_b32 m0, s11
	v_lshl_add_u64 v[144:145], s[82:83], 0, v[162:163]
	s_add_u32 s82, s82, 0x20000
	s_addc_u32 s83, s83, 0
	ds_read_b128 v[168:171], v134 offset:32768
	ds_read_b128 v[172:175], v134 offset:33792
	ds_read_b128 v[176:179], v133 offset:32768
	ds_read_b128 v[184:187], v133 offset:33792
	ds_read_b128 v[188:191], v131 offset:32768
	ds_read_b128 v[192:195], v131 offset:33792
	ds_read_b128 v[196:199], v130 offset:32768
	ds_read_b128 v[200:203], v130 offset:33792
	global_load_lds_dwordx4 v[144:145], off
	s_mov_b32 m0, s56
	v_lshl_add_u64 v[144:145], s[82:83], 0, v[162:163]
	global_load_lds_dwordx4 v[144:145], off
	s_waitcnt lgkmcnt(8)
	s_barrier
	s_setprio 1
	s_waitcnt lgkmcnt(0)
	s_bitcmp1_b32 s100, 0
	s_cbranch_scc1 .Lg2p_skip5
	v_mfma_f32_16x16x32_f16 v[102:105], v[168:171], v[140:143], v[102:105]
	v_mfma_f32_16x16x32_f16 v[98:101], v[168:171], v[158:161], v[98:101]
	v_mfma_f32_16x16x32_f16 v[126:129], v[176:179], v[140:143], v[126:129]
	v_mfma_f32_16x16x32_f16 v[122:125], v[176:179], v[158:161], v[122:125]
	v_mfma_f32_16x16x32_f16 v[118:121], v[188:191], v[140:143], v[118:121]
	v_mfma_f32_16x16x32_f16 v[114:117], v[188:191], v[158:161], v[114:117]
	v_mfma_f32_16x16x32_f16 v[110:113], v[196:199], v[140:143], v[110:113]
	v_mfma_f32_16x16x32_f16 v[106:109], v[196:199], v[158:161], v[106:109]
	v_mfma_f32_16x16x32_f16 v[102:105], v[172:175], v[154:157], v[102:105]
	v_mfma_f32_16x16x32_f16 v[98:101], v[172:175], v[164:167], v[98:101]
	v_mfma_f32_16x16x32_f16 v[126:129], v[184:187], v[154:157], v[126:129]
	v_mfma_f32_16x16x32_f16 v[122:125], v[184:187], v[164:167], v[122:125]
	v_mfma_f32_16x16x32_f16 v[118:121], v[192:195], v[154:157], v[118:121]
	v_mfma_f32_16x16x32_f16 v[114:117], v[192:195], v[164:167], v[114:117]
	v_mfma_f32_16x16x32_f16 v[110:113], v[200:203], v[154:157], v[110:113]
	v_mfma_f32_16x16x32_f16 v[106:109], v[200:203], v[164:167], v[106:109]
.Lg2p_skip5:
	s_setprio 0
	s_barrier
	s_add_u32 s78, s92, vcc_hi
	s_addc_u32 s79, s93, 0
	s_add_u32 s82, s78, 0x180
	s_addc_u32 s83, s79, 0
	s_add_i32 m0, s97, 0x18000
	v_lshl_add_u64 v[144:145], s[82:83], 0, v[162:163]
	s_add_u32 s82, s82, 0x20000
	s_addc_u32 s83, s83, 0
	ds_read_b128 v[204:207], v135
	ds_read_b128 v[208:211], v135 offset:1024
	ds_read_b128 v[212:215], v135 offset:2048
	ds_read_b128 v[216:219], v135 offset:3072
	global_load_lds_dwordx4 v[144:145], off
	s_add_i32 m0, s97, 0x1a000
	v_lshl_add_u64 v[144:145], s[82:83], 0, v[162:163]
	global_load_lds_dwordx4 v[144:145], off
	s_barrier
	s_setprio 1
	s_waitcnt lgkmcnt(0)
	s_bitcmp1_b32 s100, 0
	s_cbranch_scc1 .Lg2p_skip6
	v_mfma_f32_16x16x32_f16 v[94:97], v[168:171], v[204:207], v[94:97]
	v_mfma_f32_16x16x32_f16 v[90:93], v[168:171], v[212:215], v[90:93]
	v_mfma_f32_16x16x32_f16 v[86:89], v[176:179], v[204:207], v[86:89]
	v_mfma_f32_16x16x32_f16 v[82:85], v[176:179], v[212:215], v[82:85]
	v_mfma_f32_16x16x32_f16 v[78:81], v[188:191], v[204:207], v[78:81]
	v_mfma_f32_16x16x32_f16 v[74:77], v[188:191], v[212:215], v[74:77]
	v_mfma_f32_16x16x32_f16 v[70:73], v[196:199], v[204:207], v[70:73]
	v_mfma_f32_16x16x32_f16 v[66:69], v[196:199], v[212:215], v[66:69]
	v_mfma_f32_16x16x32_f16 v[94:97], v[172:175], v[208:211], v[94:97]
	v_mfma_f32_16x16x32_f16 v[90:93], v[172:175], v[216:219], v[90:93]
	v_mfma_f32_16x16x32_f16 v[86:89], v[184:187], v[208:211], v[86:89]
	v_mfma_f32_16x16x32_f16 v[82:85], v[184:187], v[216:219], v[82:85]
	v_mfma_f32_16x16x32_f16 v[78:81], v[192:195], v[208:211], v[78:81]
	v_mfma_f32_16x16x32_f16 v[74:77], v[192:195], v[216:219], v[74:77]
	v_mfma_f32_16x16x32_f16 v[70:73], v[200:203], v[208:211], v[70:73]
	v_mfma_f32_16x16x32_f16 v[66:69], v[200:203], v[216:219], v[66:69]
.Lg2p_skip6:
	s_setprio 0
	s_add_u32 s78, s90, vcc_hi
	s_addc_u32 s79, s91, 0
	s_add_u32 s82, s78, 0x180
	s_addc_u32 s83, s79, 0
	s_mov_b32 m0, s52
	v_lshl_add_u64 v[144:145], s[82:83], 0, v[162:163]
	s_add_u32 s82, s82, 0x20000
	s_addc_u32 s83, s83, 0
	s_barrier
	ds_read_b128 v[168:171], v134 offset:49152
	ds_read_b128 v[172:175], v134 offset:50176
	ds_read_b128 v[176:179], v133 offset:49152
	ds_read_b128 v[184:187], v133 offset:50176
	ds_read_b128 v[188:191], v131 offset:49152
	ds_read_b128 v[192:195], v131 offset:50176
	ds_read_b128 v[196:199], v130 offset:49152
	ds_read_b128 v[200:203], v130 offset:50176
	global_load_lds_dwordx4 v[144:145], off
	s_mov_b32 m0, s53
	v_lshl_add_u64 v[144:145], s[82:83], 0, v[162:163]
	global_load_lds_dwordx4 v[144:145], off
	s_barrier
	s_setprio 1
	s_waitcnt lgkmcnt(0)
	s_bitcmp1_b32 s100, 1
	s_cbranch_scc1 .Lg2p_skip7
	v_mfma_f32_16x16x32_f16 v[62:65], v[168:171], v[140:143], v[62:65]
	v_mfma_f32_16x16x32_f16 v[58:61], v[168:171], v[158:161], v[58:61]
	v_mfma_f32_16x16x32_f16 v[54:57], v[176:179], v[140:143], v[54:57]
	v_mfma_f32_16x16x32_f16 v[50:53], v[176:179], v[158:161], v[50:53]
	v_mfma_f32_16x16x32_f16 v[46:49], v[188:191], v[140:143], v[46:49]
	v_mfma_f32_16x16x32_f16 v[42:45], v[188:191], v[158:161], v[42:45]
	v_mfma_f32_16x16x32_f16 v[38:41], v[196:199], v[140:143], v[38:41]
	v_mfma_f32_16x16x32_f16 v[30:33], v[196:199], v[158:161], v[30:33]
	v_mfma_f32_16x16x32_f16 v[62:65], v[172:175], v[154:157], v[62:65]
	v_mfma_f32_16x16x32_f16 v[58:61], v[172:175], v[164:167], v[58:61]
	v_mfma_f32_16x16x32_f16 v[54:57], v[184:187], v[154:157], v[54:57]
	v_mfma_f32_16x16x32_f16 v[50:53], v[184:187], v[164:167], v[50:53]
	v_mfma_f32_16x16x32_f16 v[46:49], v[192:195], v[154:157], v[46:49]
	v_mfma_f32_16x16x32_f16 v[42:45], v[192:195], v[164:167], v[42:45]
	v_mfma_f32_16x16x32_f16 v[38:41], v[200:203], v[154:157], v[38:41]
	v_mfma_f32_16x16x32_f16 v[30:33], v[200:203], v[164:167], v[30:33]
.Lg2p_skip7:
	s_setprio 0
	s_barrier
	s_add_u32 s78, s34, vcc_hi
	s_addc_u32 s79, s35, 0
	s_add_u32 s82, s78, 0x180
	s_addc_u32 s83, s79, 0
	s_add_i32 m0, s97, 0x1c000
	v_lshl_add_u64 v[140:141], s[82:83], 0, v[162:163]
	s_add_u32 s82, s82, 0x20000
	s_addc_u32 s83, s83, 0
	global_load_lds_dwordx4 v[140:141], off
	s_add_i32 m0, s97, 0x1e000
	v_lshl_add_u64 v[140:141], s[82:83], 0, v[162:163]
	global_load_lds_dwordx4 v[140:141], off
	s_waitcnt vmcnt(6)
	s_barrier
	s_setprio 1
	s_bitcmp1_b32 s100, 1
	s_cbranch_scc1 .Lg2p_skip8
	v_mfma_f32_16x16x32_f16 v[34:37], v[168:171], v[204:207], v[34:37]
	v_mfma_f32_16x16x32_f16 v[26:29], v[168:171], v[212:215], v[26:29]
	v_mfma_f32_16x16x32_f16 v[22:25], v[176:179], v[204:207], v[22:25]
	v_mfma_f32_16x16x32_f16 v[18:21], v[176:179], v[212:215], v[18:21]
	v_mfma_f32_16x16x32_f16 v[14:17], v[188:191], v[204:207], v[14:17]
	v_mfma_f32_16x16x32_f16 v[10:13], v[188:191], v[212:215], v[10:13]
	v_mfma_f32_16x16x32_f16 v[6:9], v[196:199], v[204:207], v[6:9]
	v_mfma_f32_16x16x32_f16 v[2:5], v[196:199], v[212:215], v[2:5]
	v_mfma_f32_16x16x32_f16 v[34:37], v[172:175], v[208:211], v[34:37]
	v_mfma_f32_16x16x32_f16 v[26:29], v[172:175], v[216:219], v[26:29]
	v_mfma_f32_16x16x32_f16 v[22:25], v[184:187], v[208:211], v[22:25]
	v_mfma_f32_16x16x32_f16 v[18:21], v[184:187], v[216:219], v[18:21]
	v_mfma_f32_16x16x32_f16 v[14:17], v[192:195], v[208:211], v[14:17]
	v_mfma_f32_16x16x32_f16 v[10:13], v[192:195], v[216:219], v[10:13]
	v_mfma_f32_16x16x32_f16 v[6:9], v[200:203], v[208:211], v[6:9]
	v_mfma_f32_16x16x32_f16 v[2:5], v[200:203], v[216:219], v[2:5]
.Lg2p_skip8:
	s_setprio 0
	s_cmp_lt_u32 s57, 12
	s_mov_b32 s57, vcc_lo
	s_barrier
	s_cbranch_scc1 .Lg2p_loop
	s_add_u32 s34, s88, 0x780
	s_addc_u32 s35, s89, 0
	ds_read_b128 v[140:143], v138
	ds_read_b128 v[154:157], v138 offset:1024
	ds_read_b128 v[158:161], v138 offset:2048
	ds_read_b128 v[164:167], v138 offset:3072
	ds_read_b128 v[168:171], v134
	ds_read_b128 v[172:175], v134 offset:1024
	ds_read_b128 v[176:179], v133
	ds_read_b128 v[184:187], v133 offset:1024
	ds_read_b128 v[188:191], v131
	ds_read_b128 v[192:195], v131 offset:1024
	ds_read_b128 v[196:199], v130
	ds_read_b128 v[200:203], v130 offset:1024
	v_lshl_add_u64 v[138:139], s[34:35], 0, v[162:163]
	s_add_u32 s34, s34, 0x20000
	s_mov_b32 m0, s59
	s_addc_u32 s35, s35, 0
	global_load_lds_dwordx4 v[138:139], off
	s_mov_b32 m0, s58
	v_lshl_add_u64 v[138:139], s[34:35], 0, v[162:163]
	global_load_lds_dwordx4 v[138:139], off
	s_barrier
	s_setprio 1
	s_waitcnt lgkmcnt(0)
	s_bitcmp1_b32 s100, 0
	s_cbranch_scc1 .Lg2p_skip9
	v_mfma_f32_16x16x32_f16 v[102:105], v[168:171], v[140:143], v[102:105]
	v_mfma_f32_16x16x32_f16 v[98:101], v[168:171], v[158:161], v[98:101]
	v_mfma_f32_16x16x32_f16 v[126:129], v[176:179], v[140:143], v[126:129]
	v_mfma_f32_16x16x32_f16 v[122:125], v[176:179], v[158:161], v[122:125]
	v_mfma_f32_16x16x32_f16 v[118:121], v[188:191], v[140:143], v[118:121]
	v_mfma_f32_16x16x32_f16 v[114:117], v[188:191], v[158:161], v[114:117]
	v_mfma_f32_16x16x32_f16 v[110:113], v[196:199], v[140:143], v[110:113]
	v_mfma_f32_16x16x32_f16 v[106:109], v[196:199], v[158:161], v[106:109]
	v_mfma_f32_16x16x32_f16 v[102:105], v[172:175], v[154:157], v[102:105]
	v_mfma_f32_16x16x32_f16 v[98:101], v[172:175], v[164:167], v[98:101]
	v_mfma_f32_16x16x32_f16 v[126:129], v[184:187], v[154:157], v[126:129]
	v_mfma_f32_16x16x32_f16 v[122:125], v[184:187], v[164:167], v[122:125]
	v_mfma_f32_16x16x32_f16 v[118:121], v[192:195], v[154:157], v[118:121]
	v_mfma_f32_16x16x32_f16 v[114:117], v[192:195], v[164:167], v[114:117]
	v_mfma_f32_16x16x32_f16 v[110:113], v[200:203], v[154:157], v[110:113]
	v_mfma_f32_16x16x32_f16 v[106:109], v[200:203], v[164:167], v[106:109]
.Lg2p_skip9:
	s_setprio 0
	s_barrier
	ds_read_b128 v[204:207], v137
	ds_read_b128 v[208:211], v137 offset:1024
	ds_read_b128 v[212:215], v137 offset:2048
	ds_read_b128 v[216:219], v137 offset:3072
	s_barrier
	s_setprio 1
	s_waitcnt lgkmcnt(0)
	s_bitcmp1_b32 s100, 0
	s_cbranch_scc1 .Lg2p_skip10
	v_mfma_f32_16x16x32_f16 v[94:97], v[168:171], v[204:207], v[94:97]
	v_mfma_f32_16x16x32_f16 v[94:97], v[172:175], v[208:211], v[94:97]
	v_mfma_f32_16x16x32_f16 v[90:93], v[168:171], v[212:215], v[90:93]
	v_mfma_f32_16x16x32_f16 v[86:89], v[176:179], v[204:207], v[86:89]
	v_mfma_f32_16x16x32_f16 v[82:85], v[176:179], v[212:215], v[82:85]
	v_mfma_f32_16x16x32_f16 v[78:81], v[188:191], v[204:207], v[78:81]
	v_mfma_f32_16x16x32_f16 v[74:77], v[188:191], v[212:215], v[74:77]
	v_mfma_f32_16x16x32_f16 v[70:73], v[196:199], v[204:207], v[70:73]
	v_mfma_f32_16x16x32_f16 v[66:69], v[196:199], v[212:215], v[66:69]
	v_mfma_f32_16x16x32_f16 v[168:171], v[172:175], v[216:219], v[90:93]
	v_mfma_f32_16x16x32_f16 v[172:175], v[184:187], v[208:211], v[86:89]
	v_mfma_f32_16x16x32_f16 v[176:179], v[184:187], v[216:219], v[82:85]
	v_mfma_f32_16x16x32_f16 v[184:187], v[192:195], v[208:211], v[78:81]
	v_mfma_f32_16x16x32_f16 v[188:191], v[192:195], v[216:219], v[74:77]
	v_mfma_f32_16x16x32_f16 v[192:195], v[200:203], v[208:211], v[70:73]
	v_mfma_f32_16x16x32_f16 v[196:199], v[200:203], v[216:219], v[66:69]
.Lg2p_skip10:
	s_setprio 0
	s_barrier
	s_nop 0
	ds_read_b128 v[66:69], v134 offset:16384
	ds_read_b128 v[70:73], v134 offset:17408
	ds_read_b128 v[74:77], v133 offset:16384
	ds_read_b128 v[78:81], v133 offset:17408
	ds_read_b128 v[82:85], v131 offset:16384
	ds_read_b128 v[86:89], v131 offset:17408
	ds_read_b128 v[90:93], v130 offset:16384
	ds_read_b128 v[200:203], v130 offset:17408
	s_waitcnt vmcnt(4)
	s_barrier
	s_setprio 1
	s_waitcnt lgkmcnt(0)
	s_bitcmp1_b32 s100, 1
	s_cbranch_scc1 .Lg2p_skip11
	v_mfma_f32_16x16x32_f16 v[62:65], v[66:69], v[140:143], v[62:65]
	v_mfma_f32_16x16x32_f16 v[58:61], v[66:69], v[158:161], v[58:61]
	v_mfma_f32_16x16x32_f16 v[54:57], v[74:77], v[140:143], v[54:57]
	v_mfma_f32_16x16x32_f16 v[50:53], v[74:77], v[158:161], v[50:53]
	v_mfma_f32_16x16x32_f16 v[46:49], v[82:85], v[140:143], v[46:49]
	v_mfma_f32_16x16x32_f16 v[42:45], v[82:85], v[158:161], v[42:45]
	v_mfma_f32_16x16x32_f16 v[38:41], v[90:93], v[140:143], v[38:41]
	v_mfma_f32_16x16x32_f16 v[62:65], v[70:73], v[154:157], v[62:65]
	v_mfma_f32_16x16x32_f16 v[58:61], v[70:73], v[164:167], v[58:61]
	v_mfma_f32_16x16x32_f16 v[54:57], v[78:81], v[154:157], v[54:57]
	v_mfma_f32_16x16x32_f16 v[50:53], v[78:81], v[164:167], v[50:53]
	v_mfma_f32_16x16x32_f16 v[46:49], v[86:89], v[154:157], v[46:49]
	v_mfma_f32_16x16x32_f16 v[42:45], v[86:89], v[164:167], v[42:45]
	v_mfma_f32_16x16x32_f16 v[38:41], v[200:203], v[154:157], v[38:41]
	v_mfma_f32_16x16x32_f16 v[30:33], v[90:93], v[158:161], v[30:33]
	v_mfma_f32_16x16x32_f16 v[138:141], v[200:203], v[164:167], v[30:33]
.Lg2p_skip11:
	s_setprio 0
	s_setprio 1
	s_bitcmp1_b32 s100, 1
	s_cbranch_scc1 .Lg2p_skip12
	v_mfma_f32_16x16x32_f16 v[30:33], v[66:69], v[204:207], v[34:37]
	v_mfma_f32_16x16x32_f16 v[34:37], v[70:73], v[208:211], v[30:33]
	v_mfma_f32_16x16x32_f16 v[26:29], v[66:69], v[212:215], v[26:29]
	v_mfma_f32_16x16x32_f16 v[22:25], v[74:77], v[204:207], v[22:25]
	v_mfma_f32_16x16x32_f16 v[18:21], v[74:77], v[212:215], v[18:21]
	v_mfma_f32_16x16x32_f16 v[14:17], v[82:85], v[204:207], v[14:17]
	v_mfma_f32_16x16x32_f16 v[10:13], v[82:85], v[212:215], v[10:13]
	v_mfma_f32_16x16x32_f16 v[6:9], v[90:93], v[204:207], v[6:9]
	v_mfma_f32_16x16x32_f16 v[2:5], v[90:93], v[212:215], v[2:5]
	v_mfma_f32_16x16x32_f16 v[142:145], v[70:73], v[216:219], v[26:29]
	v_mfma_f32_16x16x32_f16 v[154:157], v[78:81], v[208:211], v[22:25]
	v_mfma_f32_16x16x32_f16 v[158:161], v[78:81], v[216:219], v[18:21]
	v_mfma_f32_16x16x32_f16 v[164:167], v[86:89], v[208:211], v[14:17]
	v_mfma_f32_16x16x32_f16 v[220:223], v[86:89], v[216:219], v[10:13]
	v_mfma_f32_16x16x32_f16 v[204:207], v[200:203], v[208:211], v[6:9]
	v_mfma_f32_16x16x32_f16 v[200:203], v[200:203], v[216:219], v[2:5]
.Lg2p_skip12:
	s_setprio 0
	s_barrier
	s_nop 0
	ds_read_b128 v[2:5], v136
	ds_read_b128 v[6:9], v136 offset:1024
	ds_read_b128 v[208:211], v136 offset:2048
	ds_read_b128 v[212:215], v136 offset:3072
	ds_read_b128 v[10:13], v134 offset:32768
	ds_read_b128 v[14:17], v134 offset:33792
	ds_read_b128 v[18:21], v133 offset:32768
	ds_read_b128 v[22:25], v133 offset:33792
	ds_read_b128 v[26:29], v131 offset:32768
	ds_read_b128 v[30:33], v131 offset:33792
	ds_read_b128 v[216:219], v130 offset:32768
	ds_read_b128 v[224:227], v130 offset:33792
	s_waitcnt vmcnt(2)
	s_barrier
	s_setprio 1
	s_waitcnt lgkmcnt(0)
	s_bitcmp1_b32 s100, 0
	s_cbranch_scc1 .Lg2p_skip13
	v_mfma_f32_16x16x32_f16 v[66:69], v[10:13], v[2:5], v[102:105]
	v_mfma_f32_16x16x32_f16 v[90:93], v[14:17], v[6:9], v[66:69]
	v_mfma_f32_16x16x32_f16 v[66:69], v[10:13], v[208:211], v[98:101]
	v_mfma_f32_16x16x32_f16 v[98:101], v[14:17], v[212:215], v[66:69]
	v_mfma_f32_16x16x32_f16 v[66:69], v[18:21], v[2:5], v[126:129]
	v_mfma_f32_16x16x32_f16 v[82:85], v[22:25], v[6:9], v[66:69]
	v_mfma_f32_16x16x32_f16 v[66:69], v[18:21], v[208:211], v[122:125]
	v_mfma_f32_16x16x32_f16 v[86:89], v[22:25], v[212:215], v[66:69]
	v_mfma_f32_16x16x32_f16 v[66:69], v[26:29], v[2:5], v[118:121]
	v_mfma_f32_16x16x32_f16 v[74:77], v[30:33], v[6:9], v[66:69]
	v_mfma_f32_16x16x32_f16 v[66:69], v[26:29], v[208:211], v[114:117]
	v_mfma_f32_16x16x32_f16 v[78:81], v[30:33], v[212:215], v[66:69]
	v_mfma_f32_16x16x32_f16 v[66:69], v[216:219], v[2:5], v[110:113]
	v_mfma_f32_16x16x32_f16 v[70:73], v[216:219], v[208:211], v[106:109]
	v_mfma_f32_16x16x32_f16 v[66:69], v[224:227], v[6:9], v[66:69]
	v_mfma_f32_16x16x32_f16 v[70:73], v[224:227], v[212:215], v[70:73]
.Lg2p_skip13:
	s_setprio 0
	s_barrier
	ds_read_b128 v[228:231], v135
	ds_read_b128 v[232:235], v135 offset:1024
	ds_read_b128 v[236:239], v135 offset:2048
	ds_read_b128 v[240:243], v135 offset:3072
	s_waitcnt vmcnt(0)
	s_barrier
	s_setprio 1
	s_waitcnt lgkmcnt(0)
	s_bitcmp1_b32 s100, 0
	s_cbranch_scc1 .Lg2p_skip14
	v_mfma_f32_16x16x32_f16 v[94:97], v[10:13], v[228:231], v[94:97]
	v_mfma_f32_16x16x32_f16 v[10:13], v[10:13], v[236:239], v[168:171]
	v_mfma_f32_16x16x32_f16 v[126:129], v[14:17], v[240:243], v[10:13]
	v_mfma_f32_16x16x32_f16 v[10:13], v[18:21], v[228:231], v[172:175]
	v_mfma_f32_16x16x32_f16 v[114:117], v[22:25], v[232:235], v[10:13]
	v_mfma_f32_16x16x32_f16 v[10:13], v[18:21], v[236:239], v[176:179]
	v_mfma_f32_16x16x32_f16 v[118:121], v[22:25], v[240:243], v[10:13]
	v_mfma_f32_16x16x32_f16 v[10:13], v[26:29], v[228:231], v[184:187]
	v_mfma_f32_16x16x32_f16 v[106:109], v[30:33], v[232:235], v[10:13]
	v_mfma_f32_16x16x32_f16 v[10:13], v[26:29], v[236:239], v[188:191]
	v_mfma_f32_16x16x32_f16 v[110:113], v[30:33], v[240:243], v[10:13]
	v_mfma_f32_16x16x32_f16 v[10:13], v[216:219], v[228:231], v[192:195]
	v_mfma_f32_16x16x32_f16 v[122:125], v[14:17], v[232:235], v[94:97]
	v_mfma_f32_16x16x32_f16 v[94:97], v[224:227], v[232:235], v[10:13]
	v_mfma_f32_16x16x32_f16 v[10:13], v[216:219], v[236:239], v[196:199]
	v_mfma_f32_16x16x32_f16 v[102:105], v[224:227], v[240:243], v[10:13]
.Lg2p_skip14:
	s_setprio 0
	s_barrier
	ds_read_b128 v[168:171], v134 offset:49152
	ds_read_b128 v[134:137], v134 offset:50176
	ds_read_b128 v[172:175], v133 offset:49152
	ds_read_b128 v[176:179], v133 offset:50176
	ds_read_b128 v[184:187], v131 offset:49152
	ds_read_b128 v[188:191], v131 offset:50176
	ds_read_b128 v[192:195], v130 offset:49152
	ds_read_b128 v[196:199], v130 offset:50176
	s_barrier
	s_setprio 1
	s_waitcnt lgkmcnt(0)
	s_bitcmp1_b32 s100, 1
	s_cbranch_scc1 .Lg2p_skip15
	v_mfma_f32_16x16x32_f16 v[10:13], v[168:171], v[2:5], v[62:65]
	v_mfma_f32_16x16x32_f16 v[26:29], v[134:137], v[6:9], v[10:13]
	v_mfma_f32_16x16x32_f16 v[10:13], v[168:171], v[208:211], v[58:61]
	v_mfma_f32_16x16x32_f16 v[30:33], v[134:137], v[212:215], v[10:13]
	v_mfma_f32_16x16x32_f16 v[10:13], v[172:175], v[2:5], v[54:57]
	v_mfma_f32_16x16x32_f16 v[18:21], v[176:179], v[6:9], v[10:13]
	v_mfma_f32_16x16x32_f16 v[10:13], v[172:175], v[208:211], v[50:53]
	v_mfma_f32_16x16x32_f16 v[22:25], v[176:179], v[212:215], v[10:13]
	v_mfma_f32_16x16x32_f16 v[10:13], v[184:187], v[2:5], v[46:49]
	v_mfma_f32_16x16x32_f16 v[2:5], v[192:195], v[2:5], v[38:41]
	v_mfma_f32_16x16x32_f16 v[10:13], v[188:191], v[6:9], v[10:13]
	v_mfma_f32_16x16x32_f16 v[14:17], v[184:187], v[208:211], v[42:45]
	v_mfma_f32_16x16x32_f16 v[2:5], v[196:199], v[6:9], v[2:5]
	v_mfma_f32_16x16x32_f16 v[6:9], v[192:195], v[208:211], v[138:141]
	v_mfma_f32_16x16x32_f16 v[14:17], v[188:191], v[212:215], v[14:17]
	v_mfma_f32_16x16x32_f16 v[6:9], v[196:199], v[212:215], v[6:9]
.Lg2p_skip15:
	s_setprio 0
	s_setprio 1
	s_bitcmp1_b32 s100, 1
	s_cbranch_scc1 .Lg2p_skip16
	v_mfma_f32_16x16x32_f16 v[34:37], v[168:171], v[228:231], v[34:37]
	v_mfma_f32_16x16x32_f16 v[58:61], v[134:137], v[232:235], v[34:37]
	v_mfma_f32_16x16x32_f16 v[34:37], v[168:171], v[236:239], v[142:145]
	v_mfma_f32_16x16x32_f16 v[62:65], v[134:137], v[240:243], v[34:37]
	v_mfma_f32_16x16x32_f16 v[34:37], v[172:175], v[228:231], v[154:157]
	v_mfma_f32_16x16x32_f16 v[50:53], v[176:179], v[232:235], v[34:37]
	v_mfma_f32_16x16x32_f16 v[34:37], v[172:175], v[236:239], v[158:161]
	v_mfma_f32_16x16x32_f16 v[54:57], v[176:179], v[240:243], v[34:37]
	v_mfma_f32_16x16x32_f16 v[34:37], v[184:187], v[228:231], v[164:167]
	v_mfma_f32_16x16x32_f16 v[42:45], v[188:191], v[232:235], v[34:37]
	v_mfma_f32_16x16x32_f16 v[34:37], v[184:187], v[236:239], v[220:223]
	v_mfma_f32_16x16x32_f16 v[46:49], v[188:191], v[240:243], v[34:37]
	v_mfma_f32_16x16x32_f16 v[34:37], v[192:195], v[228:231], v[204:207]
	v_mfma_f32_16x16x32_f16 v[38:41], v[192:195], v[236:239], v[200:203]
	v_mfma_f32_16x16x32_f16 v[34:37], v[196:199], v[232:235], v[34:37]
	v_mfma_f32_16x16x32_f16 v[38:41], v[196:199], v[240:243], v[38:41]

	.amdhsa_kernel _Z14moe_persistent8GemmArgs
		.amdhsa_group_segment_fixed_size 0
		.amdhsa_private_segment_fixed_size 0
		.amdhsa_kernarg_size 192
		.amdhsa_user_sgpr_count 2
		.amdhsa_user_sgpr_dispatch_ptr 0
		.amdhsa_user_sgpr_queue_ptr 0
		.amdhsa_user_sgpr_kernarg_segment_ptr 1
		.amdhsa_user_sgpr_dispatch_id 0
		.amdhsa_user_sgpr_kernarg_preload_length 0
		.amdhsa_user_sgpr_kernarg_preload_offset 0
		.amdhsa_user_sgpr_private_segment_size 0
		.amdhsa_uses_dynamic_stack 0
		.amdhsa_enable_private_segment 0
		.amdhsa_system_sgpr_workgroup_id_x 1
		.amdhsa_system_sgpr_workgroup_id_y 0
		.amdhsa_system_sgpr_workgroup_id_z 0
		.amdhsa_system_sgpr_workgroup_info 0
		.amdhsa_system_vgpr_workitem_id 0
		.amdhsa_next_free_vgpr 256
		.amdhsa_next_free_sgpr 102
		.amdhsa_accum_offset 256
		.amdhsa_reserve_vcc 1
		.amdhsa_float_round_mode_32 0
		.amdhsa_float_round_mode_16_64 0
		.amdhsa_float_denorm_mode_32 3
		.amdhsa_float_denorm_mode_16_64 3
		.amdhsa_dx10_clamp 1
		.amdhsa_ieee_mode 1
		.amdhsa_fp16_overflow 0
		.amdhsa_tg_split 0
		.amdhsa_exception_fp_ieee_invalid_op 0
		.amdhsa_exception_fp_denorm_src 0
		.amdhsa_exception_fp_ieee_div_zero 0
		.amdhsa_exception_fp_ieee_overflow 0
		.amdhsa_exception_fp_ieee_underflow 0
		.amdhsa_exception_fp_ieee_inexact 0
		.amdhsa_exception_int_div_zero 0
	.end_amdhsa_kernel

amdhsa.kernels:
  - .agpr_count:     0
    .args:
      - .actual_access:  read_only
        .address_space:  global
        .offset:         0
        .size:           8
        .value_kind:     global_buffer
      - .actual_access:  read_only
        .address_space:  global
        .offset:         8
        .size:           8
        .value_kind:     global_buffer
      - .actual_access:  write_only
        .address_space:  global
        .offset:         16
        .size:           8
        .value_kind:     global_buffer
      - .address_space:  global
        .offset:         24
        .size:           8
        .value_kind:     global_buffer
      - .actual_access:  write_only
        .address_space:  global
        .offset:         32
        .size:           8
        .value_kind:     global_buffer
      - .actual_access:  write_only
        .address_space:  global
        .offset:         40
        .size:           8
        .value_kind:     global_buffer
      - .actual_access:  write_only
        .address_space:  global
        .offset:         48
        .size:           8
        .value_kind:     global_buffer
    .group_segment_fixed_size: 65600
    .kernarg_segment_align: 8
    .kernarg_segment_size: 56
    .language:       OpenCL C
    .language_version:
      - 2
      - 0
    .max_flat_workgroup_size: 512
    .name:           _Z11gate_kernelPKfS0_PDF16_PiS2_PfS2_
    .private_segment_fixed_size: 0
    .sgpr_count:     83
    .sgpr_spill_count: 0
    .symbol:         _Z11gate_kernelPKfS0_PDF16_PiS2_PfS2_.kd
    .uniform_work_group_size: 1
    .uses_dynamic_stack: false
    .vgpr_count:     120
    .vgpr_spill_count: 0
    .wavefront_size: 64
  - .agpr_count:     0
    .args:
      - .actual_access:  read_only
        .address_space:  global
        .offset:         0
        .size:           8
        .value_kind:     global_buffer
      - .actual_access:  read_only
        .address_space:  global
        .offset:         8
        .size:           8
        .value_kind:     global_buffer
      - .actual_access:  write_only
        .address_space:  global
        .offset:         16
        .size:           8
        .value_kind:     global_buffer
      - .actual_access:  write_only
        .address_space:  global
        .offset:         24
        .size:           8
        .value_kind:     global_buffer
      - .actual_access:  write_only
        .address_space:  global
        .offset:         32
        .size:           8
        .value_kind:     global_buffer
    .group_segment_fixed_size: 0
    .kernarg_segment_align: 8
    .kernarg_segment_size: 40
    .language:       OpenCL C
    .language_version:
      - 2
      - 0
    .max_flat_workgroup_size: 256
    .name:           _Z11prep_kernelPKfS0_PDF16_S1_Pi
    .private_segment_fixed_size: 0
    .sgpr_count:     18
    .sgpr_spill_count: 0
    .symbol:         _Z11prep_kernelPKfS0_PDF16_S1_Pi.kd
    .uniform_work_group_size: 1
    .uses_dynamic_stack: false
    .vgpr_count:     12
    .vgpr_spill_count: 0
    .wavefront_size: 64
  - .agpr_count:     0
    .args:
      - .offset:         0
        .size:           192
        .value_kind:     by_value
    .group_segment_fixed_size: 0
    .kernarg_segment_align: 8
    .kernarg_segment_size: 192
    .language:       OpenCL C
    .language_version:
      - 2
      - 0
    .max_flat_workgroup_size: 512
    .name:           _Z14moe_persistent8GemmArgs
    .private_segment_fixed_size: 0
    .sgpr_count:     108
    .sgpr_spill_count: 57
    .symbol:         _Z14moe_persistent8GemmArgs.kd
    .uniform_work_group_size: 1
    .uses_dynamic_stack: false
    .vgpr_count:     256
    .vgpr_spill_count: 0
    .wavefront_size: 64
  - .agpr_count:     0
    .args:
      - .actual_access:  read_only
        .address_space:  global
        .offset:         0
        .size:           8
        .value_kind:     global_buffer
      - .actual_access:  read_only
        .address_space:  global
        .offset:         8
        .size:           8
        .value_kind:     global_buffer
      - .actual_access:  read_only
        .address_space:  global
        .offset:         16
        .size:           8
        .value_kind:     global_buffer
      - .actual_access:  write_only
        .address_space:  global
        .offset:         24
        .size:           8
        .value_kind:     global_buffer
    .group_segment_fixed_size: 0
    .kernarg_segment_align: 8
    .kernarg_segment_size: 32
    .language:       OpenCL C
    .language_version:
      - 2
      - 0
    .max_flat_workgroup_size: 256
    .name:           _Z14combine_kernelPKDF16_PKiS2_Pf
    .private_segment_fixed_size: 0
    .sgpr_count:     25
    .sgpr_spill_count: 0
    .symbol:         _Z14combine_kernelPKDF16_PKiS2_Pf.kd
    .uniform_work_group_size: 1
    .uses_dynamic_stack: false
    .vgpr_count:     17
    .vgpr_spill_count: 0
    .wavefront_size: 64
